# MoE fill_rows: per-unit row-index loads issued back to back, one wait, then the LDS writes
# baseline (speedup 1.0000x reference)
; #define LAS __attribute__((address_space(3)))
; __device__ __forceinline__ int mk_tid(const int wv) { int ln; asm volatile("v_mbcnt_lo_u32_b32 %0, -1, 0\n\tv_mbcnt_hi_u32_b32 %0, -1, %0" : "=v"(ln)); return wv * 64 + ln; }
; __device__ __forceinline__ void moe_tiles(const int* cnt, LAS int* tb, const int wv) {
;     if (mk_tid(wv) == 0) { int acc = 0; for (int e = 0; e < 32; ++e) { const int c = cnt[e]; tb[e] = acc; tb[33 + e] = c; acc += (c + 255) >> 8; } tb[32] = acc; }
;     __syncthreads();
; }
.LBB0_966:
	s_cmp_lt_i32 s78, 7
	s_cselect_b64 s[4:5], -1, 0
	s_and_b64 s[0:1], s[4:5], s[0:1]
	s_andn2_b64 vcc, exec, s[0:1]
	s_cbranch_vccnz .LBB0_1078
	s_and_b32 s99, s94, 7
	s_lshl_b32 s99, s99, 5
	s_lshr_b32 s94, s94, 3
	s_or_b32 s94, s94, s99
	s_mov_b32 s99, 0
	v_readlane_b32 s0, v252, 0
	s_lshl_b32 s0, s0, 6
	s_sub_i32 s0, 0, s0
	s_waitcnt vmcnt(0)
	v_mbcnt_lo_u32_b32 v0, -1, 0
	v_mbcnt_hi_u32_b32 v0, -1, v0
	s_nop 0
	v_cmp_eq_u32_e32 vcc, s0, v0
	s_and_saveexec_b64 s[0:1], vcc
	s_cbranch_execz .LBB0_969
	v_mov_b32_e32 v9, 0x4000
	s_waitcnt lgkmcnt(0)
	global_load_dwordx4 v[0:3], v9, s[76:77]
	global_load_dwordx4 v[4:7], v9, s[76:77] offset:60
	s_add_u32 s2, s76, 0x4000
	v_mov_b32_e32 v8, 0
	s_addc_u32 s3, s77, 0
	global_load_dwordx4 v[10:13], v8, s[2:3] offset:16
	global_load_dwordx4 v[14:17], v8, s[2:3] offset:32
	global_load_dwordx3 v[36:38], v8, s[2:3] offset:48
	s_add_i32 s2, 0, 0x20400
	s_add_i32 s3, 0, 0x20490
	s_add_i32 s6, 0, 0x20410
	s_add_i32 s7, 0, 0x204a0
	s_add_i32 s8, 0, 0x20420
	s_add_i32 s9, 0, 0x204b0
	v_mov_b32_e32 v39, s2
	s_add_u32 s2, s76, 0x403c
	v_mov_b32_e32 v40, s3
	s_addc_u32 s3, s77, 0
	global_load_dword v45, v9, s[76:77] offset:124
	global_load_dwordx4 v[18:21], v8, s[2:3] offset:48
	global_load_dwordx4 v[22:25], v8, s[2:3] offset:32
	global_load_dwordx4 v[26:29], v8, s[2:3] offset:16
	v_mov_b32_e32 v41, s6
	v_mov_b32_e32 v42, s7
	v_mov_b32_e32 v43, s8
	s_add_i32 s6, 0, 0x20430
	v_mov_b32_e32 v46, s6
	s_add_i32 s2, 0, 0x204c0
	v_mov_b32_e32 v44, s9
	s_waitcnt vmcnt(8)
	v_add_u32_e32 v9, 0xff, v0
	v_add_u32_e32 v31, 0xff, v1
	v_add_u32_e32 v32, 0xff, v2
	v_add_u32_e32 v33, 0xff, v3
	v_ashrrev_i32_e32 v9, 8, v9
	v_ashrrev_i32_e32 v49, 8, v31
	v_mov_b32_e32 v30, v3
	v_ashrrev_i32_e32 v50, 8, v32
	v_ashrrev_i32_e32 v51, 8, v33
	s_waitcnt vmcnt(6)
	v_add_u32_e32 v52, 0xff, v10
	v_add_u32_e32 v53, 0xff, v11
	v_mov_b32_e32 v31, v10
	v_mov_b32_e32 v32, v11
	v_mov_b32_e32 v33, v12
	v_add_u32_e32 v11, 0xff, v12
	v_add_u32_e32 v10, v49, v9
	v_add_u32_e32 v47, 0xff, v5
	ds_write_b128 v40, v[30:33]
	v_ashrrev_i32_e32 v30, 8, v11
	v_add_u32_e32 v11, v50, v10
	s_waitcnt vmcnt(5)
	v_add_u32_e32 v57, 0xff, v17
	s_waitcnt vmcnt(4)
	v_add_u32_e32 v58, 0xff, v36
	v_add_u32_e32 v59, 0xff, v37
	v_mov_b32_e32 v34, v17
	v_mov_b32_e32 v35, v36
	v_mov_b32_e32 v36, v37
	v_mov_b32_e32 v37, v38
	v_add_u32_e32 v17, 0xff, v38
	v_ashrrev_i32_e32 v38, 8, v47
	v_ashrrev_i32_e32 v47, 8, v52
	ds_write_b128 v39, v[8:11]
	v_add_u32_e32 v8, v51, v11
	v_ashrrev_i32_e32 v49, 8, v53
	v_add_u32_e32 v9, v47, v8
	v_add_u32_e32 v54, 0xff, v13
	v_add_u32_e32 v10, v49, v9
	v_add_u32_e32 v55, 0xff, v14
	v_ashrrev_i32_e32 v31, 8, v54
	v_add_u32_e32 v11, v30, v10
	v_add_u32_e32 v56, 0xff, v15
	v_ashrrev_i32_e32 v32, 8, v55
	ds_write_b128 v41, v[8:11]
	v_add_u32_e32 v8, v31, v11
	v_mov_b32_e32 v12, v13
	v_mov_b32_e32 v13, v14
	v_mov_b32_e32 v14, v15
	v_mov_b32_e32 v15, v16
	v_add_u32_e32 v16, 0xff, v16
	v_ashrrev_i32_e32 v33, 8, v56
	v_add_u32_e32 v9, v32, v8
	ds_write_b128 v42, v[12:15]
	v_ashrrev_i32_e32 v12, 8, v16
	v_add_u32_e32 v10, v33, v9
	v_ashrrev_i32_e32 v13, 8, v57
	v_add_u32_e32 v11, v12, v10
	v_ashrrev_i32_e32 v14, 8, v58
	ds_write_b128 v43, v[8:11]
	v_add_u32_e32 v8, v13, v11
	v_ashrrev_i32_e32 v15, 8, v59
	v_add_u32_e32 v9, v14, v8
	v_add_u32_e32 v3, 0xff, v4
	v_ashrrev_i32_e32 v16, 8, v17
	v_add_u32_e32 v10, v15, v9
	v_ashrrev_i32_e32 v3, 8, v3
	v_add_u32_e32 v11, v16, v10
	v_add_u32_e32 v48, 0xff, v6
	ds_write_b128 v46, v[8:11]
	v_add_u32_e32 v8, v3, v11
	v_add_u32_e32 v9, v38, v8
	v_ashrrev_i32_e32 v3, 8, v48
	v_add_u32_e32 v10, v3, v9
	v_mov_b32_e32 v3, s2
	ds_write_b128 v3, v[4:7]
	v_add_u32_e32 v3, 0xff, v7
	v_ashrrev_i32_e32 v3, 8, v3
	s_add_i32 s2, 0, 0x20440
	v_add_u32_e32 v11, v3, v10
	v_mov_b32_e32 v3, s2
	ds_write_b128 v3, v[8:11]
	s_waitcnt vmcnt(0)
	v_add_u32_e32 v3, 0xff, v26
	v_ashrrev_i32_e32 v3, 8, v3
	v_add_u32_e32 v4, v3, v11
	v_add_u32_e32 v3, 0xff, v27
	v_ashrrev_i32_e32 v3, 8, v3
	v_add_u32_e32 v5, v3, v4
	v_add_u32_e32 v3, 0xff, v28
	v_ashrrev_i32_e32 v3, 8, v3
	s_add_i32 s2, 0, 0x204d0
	v_add_u32_e32 v6, v3, v5
	v_mov_b32_e32 v3, s2
	ds_write_b128 v3, v[26:29]
	v_add_u32_e32 v3, 0xff, v29
	v_ashrrev_i32_e32 v3, 8, v3
	s_add_i32 s2, 0, 0x20450
	v_add_u32_e32 v7, v3, v6
	v_mov_b32_e32 v3, s2
	ds_write_b128 v3, v[4:7]
	v_add_u32_e32 v3, 0xff, v22
	v_ashrrev_i32_e32 v3, 8, v3
	v_add_u32_e32 v4, v3, v7
	v_add_u32_e32 v3, 0xff, v23
	v_ashrrev_i32_e32 v3, 8, v3
	v_add_u32_e32 v5, v3, v4
	v_add_u32_e32 v3, 0xff, v24
	v_ashrrev_i32_e32 v3, 8, v3
	s_add_i32 s2, 0, 0x204e0
	v_add_u32_e32 v6, v3, v5
	v_mov_b32_e32 v3, s2
	ds_write_b128 v3, v[22:25]
	v_add_u32_e32 v3, 0xff, v25
	v_ashrrev_i32_e32 v3, 8, v3
	s_add_i32 s2, 0, 0x20460
	v_add_u32_e32 v7, v3, v6
	v_mov_b32_e32 v3, s2
	ds_write_b128 v3, v[4:7]
	v_add_u32_e32 v3, 0xff, v18
	v_ashrrev_i32_e32 v3, 8, v3
	v_add_u32_e32 v4, v3, v7
	v_add_u32_e32 v3, 0xff, v19
	v_ashrrev_i32_e32 v3, 8, v3
	v_add_u32_e32 v5, v3, v4
	v_add_u32_e32 v3, 0xff, v20
	v_ashrrev_i32_e32 v3, 8, v3
	s_add_i32 s2, 0, 0x204f0
	v_add_u32_e32 v6, v3, v5
	v_mov_b32_e32 v3, s2
	ds_write_b128 v3, v[18:21]
	v_add_u32_e32 v3, 0xff, v21
	v_ashrrev_i32_e32 v3, 8, v3
	s_add_i32 s2, 0, 0x20470
	v_add_u32_e32 v7, v3, v6
	v_mov_b32_e32 v3, s2
	s_add_i32 s2, 0, 0x20500
	ds_write_b128 v3, v[4:7]
	v_mov_b32_e32 v3, s2
	ds_write_b32 v3, v45
	v_add_u32_e32 v3, 0xff, v45
	v_ashrrev_i32_e32 v3, 8, v3
	s_add_i32 s2, 0, 0x20480
	v_add_u32_e32 v4, v3, v7
	v_mov_b32_e32 v5, v0
	v_mov_b32_e32 v6, v1
	v_mov_b32_e32 v7, v2
	v_mov_b32_e32 v0, s2
	ds_write_b128 v44, v[34:37]
	ds_write_b128 v0, v[4:7]
;     __device__ __forceinline__ const char* bptr(const Unit& u) const { return (const char*)Bt + (size_t)u.pn * 256 * K * 2; }
;     __device__ __forceinline__ unsigned arow(const Unit& u, int r) const { return (unsigned)(u.pm * 256 + r); }
;     __device__ __forceinline__ bool next(int i, Unit& u) const {
;         const int L = i * G + c, total = tb[32] * 8; if (L >= total || i >= 8) return false;
;         const int mt = L >> 3; int e = 0;
;         for (int j = 1; j < 32; ++j) e = (tb[j] <= mt) ? j : e;
;         e = __builtin_amdgcn_readfirstlane(e);
;         u.e = e; u.pm = mt - tb[e]; u.pn = L & 7; u.ui = i;
;         const int rem = tb[33 + e] - u.pm * 256; u.rows = rem < 256 ? rem : 256; return true;
;     }
;     __device__ __forceinline__ const char* bptr(const Unit& u) const { return (const char*)Bt + ((size_t)u.e * 2048 + (size_t)u.pn * 256) * K * 2; }
;     __device__ __forceinline__ unsigned arow(const Unit& u, int r) const { return (unsigned)(rowtab[u.ui * 256 + r] >> a_shift); }
;     __device__ __forceinline__ void fill_rows(const int tid) const {
;         Unit u;
;         for (int i = 0; i < 8 && next(i, u); ++i)
;             if (tid < 256) rowtab[i * 256 + tid] = slot[(size_t)u.e * ECAP + u.pm * 256 + (tid < u.rows ? tid : 0)];
;         __syncthreads();
.LBB0_969:
	s_or_b64 exec, exec, s[0:1]
	s_add_i32 s0, 0, 0x20480
	v_mov_b32_e32 v1, s0
	s_waitcnt lgkmcnt(0)
	s_barrier
	v_mbcnt_lo_u32_b32 v0, -1, 0
	v_mbcnt_hi_u32_b32 v0, -1, v0
	ds_read_b32 v1, v1
	s_waitcnt lgkmcnt(0)
	v_lshlrev_b32_e32 v2, 3, v1
	v_cmp_ge_i32_e32 vcc, s94, v2
	s_cbranch_vccnz .LBB0_994
	s_add_u32 s8, s76, 0x5e188000
	v_add_u32_e32 v1, s92, v0
	s_movk_i32 s0, 0x100
	s_addc_u32 s9, s77, 0
	v_cmp_gt_i32_e32 vcc, s0, v1
	s_add_i32 s0, 0, 0x20800
	v_lshl_add_u32 v0, v1, 2, s0
	s_add_i32 s0, 0, 0x20404
	v_mov_b32_e32 v3, s0
	ds_read2_b32 v[4:5], v3 offset1:1
	s_add_i32 s0, 0, 0x2040c
	v_mov_b32_e32 v3, s0
	s_add_i32 s0, 0, 0x20414
	v_mov_b32_e32 v8, s0
	s_add_i32 s0, 0, 0x2041c
	v_mov_b32_e32 v10, s0
	s_ashr_i32 s6, s94, 3
	ds_read2_b32 v[6:7], v3 offset1:1
	ds_read2_b32 v[8:9], v8 offset1:1
	ds_read2_b32 v[10:11], v10 offset1:1
	s_waitcnt lgkmcnt(3)
	v_cmp_ge_i32_e64 s[0:1], s6, v4
	s_nop 1
	v_cndmask_b32_e64 v3, 0, 1, s[0:1]
	v_cmp_lt_i32_e64 s[0:1], s6, v5
	s_nop 1
	v_cndmask_b32_e64 v3, 2, v3, s[0:1]
	s_waitcnt lgkmcnt(2)
	v_cmp_lt_i32_e64 s[0:1], s6, v6
	s_nop 1
	v_cndmask_b32_e64 v3, 3, v3, s[0:1]
	v_cmp_lt_i32_e64 s[0:1], s6, v7
	s_nop 1
	v_cndmask_b32_e64 v3, 4, v3, s[0:1]
	s_waitcnt lgkmcnt(1)
	v_cmp_lt_i32_e64 s[0:1], s6, v8
	s_nop 1
	v_cndmask_b32_e64 v3, 5, v3, s[0:1]
	v_cmp_lt_i32_e64 s[0:1], s6, v9
	s_nop 1
	v_cndmask_b32_e64 v3, 6, v3, s[0:1]
	s_waitcnt lgkmcnt(0)
	v_cmp_lt_i32_e64 s[0:1], s6, v10
	s_nop 1
	v_cndmask_b32_e64 v3, 7, v3, s[0:1]
	v_cmp_lt_i32_e64 s[0:1], s6, v11
	s_nop 1
	v_cndmask_b32_e64 v3, 8, v3, s[0:1]
	s_add_i32 s0, 0, 0x20424
	v_mov_b32_e32 v4, s0
	ds_read2_b32 v[4:5], v4 offset1:1
	s_add_i32 s0, 0, 0x2042c
	v_mov_b32_e32 v6, s0
	s_add_i32 s0, 0, 0x20434
	v_mov_b32_e32 v8, s0
	s_add_i32 s0, 0, 0x2043c
	v_mov_b32_e32 v10, s0
	ds_read2_b32 v[6:7], v6 offset1:1
	ds_read2_b32 v[8:9], v8 offset1:1
	ds_read2_b32 v[10:11], v10 offset1:1
	s_waitcnt lgkmcnt(3)
	v_cmp_lt_i32_e64 s[0:1], s6, v4
	s_nop 1
	v_cndmask_b32_e64 v3, 9, v3, s[0:1]
	v_cmp_lt_i32_e64 s[0:1], s6, v5
	s_nop 1
	v_cndmask_b32_e64 v3, 10, v3, s[0:1]
	s_waitcnt lgkmcnt(2)
	v_cmp_lt_i32_e64 s[0:1], s6, v6
	s_nop 1
	v_cndmask_b32_e64 v3, 11, v3, s[0:1]
	v_cmp_lt_i32_e64 s[0:1], s6, v7
	s_nop 1
	v_cndmask_b32_e64 v3, 12, v3, s[0:1]
	s_waitcnt lgkmcnt(1)
	v_cmp_lt_i32_e64 s[0:1], s6, v8
	s_nop 1
	v_cndmask_b32_e64 v3, 13, v3, s[0:1]
	v_cmp_lt_i32_e64 s[0:1], s6, v9
	s_nop 1
	v_cndmask_b32_e64 v3, 14, v3, s[0:1]
	s_waitcnt lgkmcnt(0)
	v_cmp_lt_i32_e64 s[0:1], s6, v10
	s_nop 1
	v_cndmask_b32_e64 v3, 15, v3, s[0:1]
	v_cmp_lt_i32_e64 s[0:1], s6, v11
	s_nop 1
	v_cndmask_b32_e64 v3, 16, v3, s[0:1]
	s_add_i32 s0, 0, 0x20444
	v_mov_b32_e32 v4, s0
	ds_read2_b32 v[4:5], v4 offset1:1
	s_add_i32 s0, 0, 0x2044c
	v_mov_b32_e32 v6, s0
	s_add_i32 s0, 0, 0x20454
	v_mov_b32_e32 v8, s0
	s_add_i32 s0, 0, 0x2045c
	v_mov_b32_e32 v10, s0
	ds_read2_b32 v[6:7], v6 offset1:1
	ds_read2_b32 v[8:9], v8 offset1:1
	ds_read2_b32 v[10:11], v10 offset1:1
	s_waitcnt lgkmcnt(3)
	v_cmp_lt_i32_e64 s[0:1], s6, v4
	s_nop 1
	v_cndmask_b32_e64 v3, 17, v3, s[0:1]
	v_cmp_lt_i32_e64 s[0:1], s6, v5
	s_nop 1
	v_cndmask_b32_e64 v3, 18, v3, s[0:1]
	s_waitcnt lgkmcnt(2)
	v_cmp_lt_i32_e64 s[0:1], s6, v6
	s_nop 1
	v_cndmask_b32_e64 v3, 19, v3, s[0:1]
	v_cmp_lt_i32_e64 s[0:1], s6, v7
	s_nop 1
	v_cndmask_b32_e64 v3, 20, v3, s[0:1]
	s_waitcnt lgkmcnt(1)
	v_cmp_lt_i32_e64 s[0:1], s6, v8
	s_nop 1
	v_cndmask_b32_e64 v3, 21, v3, s[0:1]
	v_cmp_lt_i32_e64 s[0:1], s6, v9
	s_nop 1
	v_cndmask_b32_e64 v3, 22, v3, s[0:1]
	s_waitcnt lgkmcnt(0)
	v_cmp_lt_i32_e64 s[0:1], s6, v10
	s_nop 1
	v_cndmask_b32_e64 v3, 23, v3, s[0:1]
	v_cmp_lt_i32_e64 s[0:1], s6, v11
	s_nop 1
	v_cndmask_b32_e64 v3, 24, v3, s[0:1]
	s_add_i32 s0, 0, 0x20464
	v_mov_b32_e32 v4, s0
	ds_read2_b32 v[4:5], v4 offset1:1
	s_add_i32 s0, 0, 0x2046c
	v_mov_b32_e32 v6, s0
	s_add_i32 s0, 0, 0x20474
	v_mov_b32_e32 v8, s0
	s_add_i32 s0, 0, 0x2047c
	v_mov_b32_e32 v10, s0
	ds_read2_b32 v[6:7], v6 offset1:1
	ds_read2_b32 v[8:9], v8 offset1:1
	ds_read_b32 v10, v10
	s_waitcnt lgkmcnt(3)
	v_cmp_lt_i32_e64 s[0:1], s6, v4
	s_nop 1
	v_cndmask_b32_e64 v3, 25, v3, s[0:1]
	v_cmp_lt_i32_e64 s[0:1], s6, v5
	s_nop 1
	v_cndmask_b32_e64 v3, 26, v3, s[0:1]
	s_waitcnt lgkmcnt(2)
	v_cmp_lt_i32_e64 s[0:1], s6, v6
	s_nop 1
	v_cndmask_b32_e64 v3, 27, v3, s[0:1]
	v_cmp_lt_i32_e64 s[0:1], s6, v7
	s_nop 1
	v_cndmask_b32_e64 v3, 28, v3, s[0:1]
	s_waitcnt lgkmcnt(1)
	v_cmp_lt_i32_e64 s[0:1], s6, v8
	s_nop 1
	v_cndmask_b32_e64 v3, 29, v3, s[0:1]
	v_cmp_lt_i32_e64 s[0:1], s6, v9
	s_nop 1
	v_cndmask_b32_e64 v3, 30, v3, s[0:1]
	s_waitcnt lgkmcnt(0)
	v_cmp_lt_i32_e64 s[0:1], s6, v10
	s_nop 1
	v_cndmask_b32_e64 v3, 31, v3, s[0:1]
	s_nop 0
	v_readfirstlane_b32 s0, v3
	s_and_saveexec_b64 s[2:3], vcc
	s_cbranch_execz .LBB0_972
	s_lshl_b32 s1, s0, 2
	s_add_i32 s1, s1, 0
	s_add_i32 s1, s1, 0x20400
	v_mov_b32_e32 v2, s1
	ds_read2_b32 v[2:3], v2 offset1:33
	s_ashr_i32 s1, s0, 31
	s_lshl_b64 s[10:11], s[0:1], 16
	s_waitcnt lgkmcnt(0)
	v_readfirstlane_b32 s0, v2
	s_sub_i32 s0, s6, s0
	s_lshl_b32 s6, s0, 8
	v_subrev_u32_e32 v2, s6, v3
	s_ashr_i32 s7, s6, 31
	v_cmp_gt_i32_e64 s[0:1], v2, v1
	s_add_u32 s10, s8, s10
	s_addc_u32 s11, s9, s11
	v_cndmask_b32_e64 v2, 0, v1, s[0:1]
	s_lshl_b64 s[0:1], s[6:7], 2
	s_add_u32 s0, s10, s0
	v_ashrrev_i32_e32 v3, 31, v2
	s_addc_u32 s1, s11, s1
	v_lshl_add_u64 v[2:3], v[2:3], 2, s[0:1]
	global_load_dword v244, v[2:3], off
	s_bitset1_b32 s99, 0
	s_add_i32 s0, 0, 0x20480
	v_mov_b32_e32 v2, s0
	ds_read_b32 v2, v2
	s_waitcnt lgkmcnt(0)
	v_lshlrev_b32_e32 v2, 3, v2
;     __device__ __forceinline__ const char* bptr(const Unit& u) const { return (const char*)Bt + (size_t)u.pn * 256 * K * 2; }
;     __device__ __forceinline__ unsigned arow(const Unit& u, int r) const { return (unsigned)(u.pm * 256 + r); }
;     __device__ __forceinline__ bool next(int i, Unit& u) const {
;         const int L = i * G + c, total = tb[32] * 8; if (L >= total || i >= 8) return false;
;         const int mt = L >> 3; int e = 0;
;         for (int j = 1; j < 32; ++j) e = (tb[j] <= mt) ? j : e;
;         e = __builtin_amdgcn_readfirstlane(e);
;         u.e = e; u.pm = mt - tb[e]; u.pn = L & 7; u.ui = i;
;         const int rem = tb[33 + e] - u.pm * 256; u.rows = rem < 256 ? rem : 256; return true;
;     }
;     __device__ __forceinline__ const char* bptr(const Unit& u) const { return (const char*)Bt + ((size_t)u.e * 2048 + (size_t)u.pn * 256) * K * 2; }
;     __device__ __forceinline__ unsigned arow(const Unit& u, int r) const { return (unsigned)(rowtab[u.ui * 256 + r] >> a_shift); }
;     __device__ __forceinline__ void fill_rows(const int tid) const {
;         Unit u;
;         for (int i = 0; i < 8 && next(i, u); ++i)
;             if (tid < 256) rowtab[i * 256 + tid] = slot[(size_t)u.e * ECAP + u.pm * 256 + (tid < u.rows ? tid : 0)];
;         __syncthreads();
.LBB0_972:
	s_or_b64 exec, exec, s[2:3]
	s_add_i32 s10, s93, s94
	v_cmp_lt_i32_e64 s[0:1], s10, v2
	s_and_saveexec_b64 s[2:3], s[0:1]
	s_cbranch_execz .LBB0_993
	s_add_i32 s0, 0, 0x20404
	v_mov_b32_e32 v3, s0
	ds_read2_b32 v[4:5], v3 offset1:1
	s_add_i32 s0, 0, 0x2040c
	v_mov_b32_e32 v3, s0
	s_add_i32 s0, 0, 0x20414
	v_mov_b32_e32 v8, s0
	s_add_i32 s0, 0, 0x2041c
	v_mov_b32_e32 v10, s0
	s_ashr_i32 s11, s10, 3
	ds_read2_b32 v[6:7], v3 offset1:1
	ds_read2_b32 v[8:9], v8 offset1:1
	ds_read2_b32 v[10:11], v10 offset1:1
	s_waitcnt lgkmcnt(3)
	v_cmp_ge_i32_e64 s[0:1], s11, v4
	s_nop 1
	v_cndmask_b32_e64 v3, 0, 1, s[0:1]
	v_cmp_lt_i32_e64 s[0:1], s11, v5
	s_nop 1
	v_cndmask_b32_e64 v3, 2, v3, s[0:1]
	s_waitcnt lgkmcnt(2)
	v_cmp_lt_i32_e64 s[0:1], s11, v6
	s_nop 1
	v_cndmask_b32_e64 v3, 3, v3, s[0:1]
	v_cmp_lt_i32_e64 s[0:1], s11, v7
	s_nop 1
	v_cndmask_b32_e64 v3, 4, v3, s[0:1]
	s_waitcnt lgkmcnt(1)
	v_cmp_lt_i32_e64 s[0:1], s11, v8
	s_nop 1
	v_cndmask_b32_e64 v3, 5, v3, s[0:1]
	v_cmp_lt_i32_e64 s[0:1], s11, v9
	s_nop 1
	v_cndmask_b32_e64 v3, 6, v3, s[0:1]
	s_waitcnt lgkmcnt(0)
	v_cmp_lt_i32_e64 s[0:1], s11, v10
	s_nop 1
	v_cndmask_b32_e64 v3, 7, v3, s[0:1]
	v_cmp_lt_i32_e64 s[0:1], s11, v11
	s_nop 1
	v_cndmask_b32_e64 v3, 8, v3, s[0:1]
	s_add_i32 s0, 0, 0x20424
	v_mov_b32_e32 v4, s0
	ds_read2_b32 v[4:5], v4 offset1:1
	s_add_i32 s0, 0, 0x2042c
	v_mov_b32_e32 v6, s0
	s_add_i32 s0, 0, 0x20434
	v_mov_b32_e32 v8, s0
	s_add_i32 s0, 0, 0x2043c
	v_mov_b32_e32 v10, s0
	ds_read2_b32 v[6:7], v6 offset1:1
	ds_read2_b32 v[8:9], v8 offset1:1
	ds_read2_b32 v[10:11], v10 offset1:1
	s_waitcnt lgkmcnt(3)
	v_cmp_lt_i32_e64 s[0:1], s11, v4
	s_nop 1
	v_cndmask_b32_e64 v3, 9, v3, s[0:1]
	v_cmp_lt_i32_e64 s[0:1], s11, v5
	s_nop 1
	v_cndmask_b32_e64 v3, 10, v3, s[0:1]
	s_waitcnt lgkmcnt(2)
	v_cmp_lt_i32_e64 s[0:1], s11, v6
	s_nop 1
	v_cndmask_b32_e64 v3, 11, v3, s[0:1]
	v_cmp_lt_i32_e64 s[0:1], s11, v7
	s_nop 1
	v_cndmask_b32_e64 v3, 12, v3, s[0:1]
	s_waitcnt lgkmcnt(1)
	v_cmp_lt_i32_e64 s[0:1], s11, v8
	s_nop 1
	v_cndmask_b32_e64 v3, 13, v3, s[0:1]
	v_cmp_lt_i32_e64 s[0:1], s11, v9
	s_nop 1
	v_cndmask_b32_e64 v3, 14, v3, s[0:1]
	s_waitcnt lgkmcnt(0)
	v_cmp_lt_i32_e64 s[0:1], s11, v10
	s_nop 1
	v_cndmask_b32_e64 v3, 15, v3, s[0:1]
	v_cmp_lt_i32_e64 s[0:1], s11, v11
	s_nop 1
	v_cndmask_b32_e64 v3, 16, v3, s[0:1]
	s_add_i32 s0, 0, 0x20444
	v_mov_b32_e32 v4, s0
	ds_read2_b32 v[4:5], v4 offset1:1
	s_add_i32 s0, 0, 0x2044c
	v_mov_b32_e32 v6, s0
	s_add_i32 s0, 0, 0x20454
	v_mov_b32_e32 v8, s0
	s_add_i32 s0, 0, 0x2045c
	v_mov_b32_e32 v10, s0
	ds_read2_b32 v[6:7], v6 offset1:1
	ds_read2_b32 v[8:9], v8 offset1:1
	ds_read2_b32 v[10:11], v10 offset1:1
	s_waitcnt lgkmcnt(3)
	v_cmp_lt_i32_e64 s[0:1], s11, v4
	s_nop 1
	v_cndmask_b32_e64 v3, 17, v3, s[0:1]
	v_cmp_lt_i32_e64 s[0:1], s11, v5
	s_nop 1
	v_cndmask_b32_e64 v3, 18, v3, s[0:1]
	s_waitcnt lgkmcnt(2)
	v_cmp_lt_i32_e64 s[0:1], s11, v6
	s_nop 1
	v_cndmask_b32_e64 v3, 19, v3, s[0:1]
	v_cmp_lt_i32_e64 s[0:1], s11, v7
	s_nop 1
	v_cndmask_b32_e64 v3, 20, v3, s[0:1]
	s_waitcnt lgkmcnt(1)
	v_cmp_lt_i32_e64 s[0:1], s11, v8
	s_nop 1
	v_cndmask_b32_e64 v3, 21, v3, s[0:1]
	v_cmp_lt_i32_e64 s[0:1], s11, v9
	s_nop 1
	v_cndmask_b32_e64 v3, 22, v3, s[0:1]
	s_waitcnt lgkmcnt(0)
	v_cmp_lt_i32_e64 s[0:1], s11, v10
	s_nop 1
	v_cndmask_b32_e64 v3, 23, v3, s[0:1]
	v_cmp_lt_i32_e64 s[0:1], s11, v11
	s_nop 1
	v_cndmask_b32_e64 v3, 24, v3, s[0:1]
	s_add_i32 s0, 0, 0x20464
	v_mov_b32_e32 v4, s0
	ds_read2_b32 v[4:5], v4 offset1:1
	s_add_i32 s0, 0, 0x2046c
	v_mov_b32_e32 v6, s0
	s_add_i32 s0, 0, 0x20474
	v_mov_b32_e32 v8, s0
	s_add_i32 s0, 0, 0x2047c
	v_mov_b32_e32 v10, s0
	ds_read2_b32 v[6:7], v6 offset1:1
	ds_read2_b32 v[8:9], v8 offset1:1
	ds_read_b32 v10, v10
	s_waitcnt lgkmcnt(3)
	v_cmp_lt_i32_e64 s[0:1], s11, v4
	s_nop 1
	v_cndmask_b32_e64 v3, 25, v3, s[0:1]
	v_cmp_lt_i32_e64 s[0:1], s11, v5
	s_nop 1
	v_cndmask_b32_e64 v3, 26, v3, s[0:1]
	s_waitcnt lgkmcnt(2)
	v_cmp_lt_i32_e64 s[0:1], s11, v6
	s_nop 1
	v_cndmask_b32_e64 v3, 27, v3, s[0:1]
	v_cmp_lt_i32_e64 s[0:1], s11, v7
	s_nop 1
	v_cndmask_b32_e64 v3, 28, v3, s[0:1]
	s_waitcnt lgkmcnt(1)
	v_cmp_lt_i32_e64 s[0:1], s11, v8
	s_nop 1
	v_cndmask_b32_e64 v3, 29, v3, s[0:1]
	v_cmp_lt_i32_e64 s[0:1], s11, v9
	s_nop 1
	v_cndmask_b32_e64 v3, 30, v3, s[0:1]
	s_waitcnt lgkmcnt(0)
	v_cmp_lt_i32_e64 s[0:1], s11, v10
	s_nop 1
	v_cndmask_b32_e64 v3, 31, v3, s[0:1]
	s_nop 0
	v_readfirstlane_b32 s0, v3
	s_and_saveexec_b64 s[6:7], vcc
	s_cbranch_execz .LBB0_975
	s_lshl_b32 s1, s0, 2
	s_add_i32 s1, s1, 0
	s_add_i32 s1, s1, 0x20400
	v_mov_b32_e32 v2, s1
	ds_read2_b32 v[2:3], v2 offset1:33
	s_ashr_i32 s1, s0, 31
	s_lshl_b64 s[12:13], s[0:1], 16
	s_waitcnt lgkmcnt(0)
	v_readfirstlane_b32 s0, v2
	s_sub_i32 s0, s11, s0
	s_lshl_b32 s14, s0, 8
	v_subrev_u32_e32 v2, s14, v3
	s_ashr_i32 s15, s14, 31
	v_cmp_gt_i32_e64 s[0:1], v2, v1
	s_add_u32 s11, s8, s12
	s_addc_u32 s12, s9, s13
	v_cndmask_b32_e64 v2, 0, v1, s[0:1]
	s_lshl_b64 s[0:1], s[14:15], 2
	s_add_u32 s0, s11, s0
	v_ashrrev_i32_e32 v3, 31, v2
	s_addc_u32 s1, s12, s1
	v_lshl_add_u64 v[2:3], v[2:3], 2, s[0:1]
	global_load_dword v245, v[2:3], off
	s_bitset1_b32 s99, 1
	s_add_i32 s0, 0, 0x20480
	v_mov_b32_e32 v2, s0
	ds_read_b32 v2, v2
	s_waitcnt lgkmcnt(0)
	v_lshlrev_b32_e32 v2, 3, v2
;     __device__ __forceinline__ const char* bptr(const Unit& u) const { return (const char*)Bt + (size_t)u.pn * 256 * K * 2; }
;     __device__ __forceinline__ unsigned arow(const Unit& u, int r) const { return (unsigned)(u.pm * 256 + r); }
;     __device__ __forceinline__ bool next(int i, Unit& u) const {
;         const int L = i * G + c, total = tb[32] * 8; if (L >= total || i >= 8) return false;
;         const int mt = L >> 3; int e = 0;
;         for (int j = 1; j < 32; ++j) e = (tb[j] <= mt) ? j : e;
;         e = __builtin_amdgcn_readfirstlane(e);
;         u.e = e; u.pm = mt - tb[e]; u.pn = L & 7; u.ui = i;
;         const int rem = tb[33 + e] - u.pm * 256; u.rows = rem < 256 ? rem : 256; return true;
;     }
;     __device__ __forceinline__ const char* bptr(const Unit& u) const { return (const char*)Bt + ((size_t)u.e * 2048 + (size_t)u.pn * 256) * K * 2; }
;     __device__ __forceinline__ unsigned arow(const Unit& u, int r) const { return (unsigned)(rowtab[u.ui * 256 + r] >> a_shift); }
;     __device__ __forceinline__ void fill_rows(const int tid) const {
;         Unit u;
;         for (int i = 0; i < 8 && next(i, u); ++i)
;             if (tid < 256) rowtab[i * 256 + tid] = slot[(size_t)u.e * ECAP + u.pm * 256 + (tid < u.rows ? tid : 0)];
;         __syncthreads();
.LBB0_975:
	s_or_b64 exec, exec, s[6:7]
	s_add_i32 s10, s10, s93
	v_cmp_lt_i32_e64 s[0:1], s10, v2
	s_and_b64 exec, exec, s[0:1]
	s_cbranch_execz .LBB0_993
	s_add_i32 s0, 0, 0x20404
	v_mov_b32_e32 v3, s0
	ds_read2_b32 v[4:5], v3 offset1:1
	s_add_i32 s0, 0, 0x2040c
	v_mov_b32_e32 v3, s0
	s_add_i32 s0, 0, 0x20414
	v_mov_b32_e32 v8, s0
	s_add_i32 s0, 0, 0x2041c
	v_mov_b32_e32 v10, s0
	s_ashr_i32 s11, s10, 3
	ds_read2_b32 v[6:7], v3 offset1:1
	ds_read2_b32 v[8:9], v8 offset1:1
	ds_read2_b32 v[10:11], v10 offset1:1
	s_waitcnt lgkmcnt(3)
	v_cmp_ge_i32_e64 s[0:1], s11, v4
	s_nop 1
	v_cndmask_b32_e64 v3, 0, 1, s[0:1]
	v_cmp_lt_i32_e64 s[0:1], s11, v5
	s_nop 1
	v_cndmask_b32_e64 v3, 2, v3, s[0:1]
	s_waitcnt lgkmcnt(2)
	v_cmp_lt_i32_e64 s[0:1], s11, v6
	s_nop 1
	v_cndmask_b32_e64 v3, 3, v3, s[0:1]
	v_cmp_lt_i32_e64 s[0:1], s11, v7
	s_nop 1
	v_cndmask_b32_e64 v3, 4, v3, s[0:1]
	s_waitcnt lgkmcnt(1)
	v_cmp_lt_i32_e64 s[0:1], s11, v8
	s_nop 1
	v_cndmask_b32_e64 v3, 5, v3, s[0:1]
	v_cmp_lt_i32_e64 s[0:1], s11, v9
	s_nop 1
	v_cndmask_b32_e64 v3, 6, v3, s[0:1]
	s_waitcnt lgkmcnt(0)
	v_cmp_lt_i32_e64 s[0:1], s11, v10
	s_nop 1
	v_cndmask_b32_e64 v3, 7, v3, s[0:1]
	v_cmp_lt_i32_e64 s[0:1], s11, v11
	s_nop 1
	v_cndmask_b32_e64 v3, 8, v3, s[0:1]
	s_add_i32 s0, 0, 0x20424
	v_mov_b32_e32 v4, s0
	ds_read2_b32 v[4:5], v4 offset1:1
	s_add_i32 s0, 0, 0x2042c
	v_mov_b32_e32 v6, s0
	s_add_i32 s0, 0, 0x20434
	v_mov_b32_e32 v8, s0
	s_add_i32 s0, 0, 0x2043c
	v_mov_b32_e32 v10, s0
	ds_read2_b32 v[6:7], v6 offset1:1
	ds_read2_b32 v[8:9], v8 offset1:1
	ds_read2_b32 v[10:11], v10 offset1:1
	s_waitcnt lgkmcnt(3)
	v_cmp_lt_i32_e64 s[0:1], s11, v4
	s_nop 1
	v_cndmask_b32_e64 v3, 9, v3, s[0:1]
	v_cmp_lt_i32_e64 s[0:1], s11, v5
	s_nop 1
	v_cndmask_b32_e64 v3, 10, v3, s[0:1]
	s_waitcnt lgkmcnt(2)
	v_cmp_lt_i32_e64 s[0:1], s11, v6
	s_nop 1
	v_cndmask_b32_e64 v3, 11, v3, s[0:1]
	v_cmp_lt_i32_e64 s[0:1], s11, v7
	s_nop 1
	v_cndmask_b32_e64 v3, 12, v3, s[0:1]
	s_waitcnt lgkmcnt(1)
	v_cmp_lt_i32_e64 s[0:1], s11, v8
	s_nop 1
	v_cndmask_b32_e64 v3, 13, v3, s[0:1]
	v_cmp_lt_i32_e64 s[0:1], s11, v9
	s_nop 1
	v_cndmask_b32_e64 v3, 14, v3, s[0:1]
	s_waitcnt lgkmcnt(0)
	v_cmp_lt_i32_e64 s[0:1], s11, v10
	s_nop 1
	v_cndmask_b32_e64 v3, 15, v3, s[0:1]
	v_cmp_lt_i32_e64 s[0:1], s11, v11
	s_nop 1
	v_cndmask_b32_e64 v3, 16, v3, s[0:1]
	s_add_i32 s0, 0, 0x20444
	v_mov_b32_e32 v4, s0
	ds_read2_b32 v[4:5], v4 offset1:1
	s_add_i32 s0, 0, 0x2044c
	v_mov_b32_e32 v6, s0
	s_add_i32 s0, 0, 0x20454
	v_mov_b32_e32 v8, s0
	s_add_i32 s0, 0, 0x2045c
	v_mov_b32_e32 v10, s0
	ds_read2_b32 v[6:7], v6 offset1:1
	ds_read2_b32 v[8:9], v8 offset1:1
	ds_read2_b32 v[10:11], v10 offset1:1
	s_waitcnt lgkmcnt(3)
	v_cmp_lt_i32_e64 s[0:1], s11, v4
	s_nop 1
	v_cndmask_b32_e64 v3, 17, v3, s[0:1]
	v_cmp_lt_i32_e64 s[0:1], s11, v5
	s_nop 1
	v_cndmask_b32_e64 v3, 18, v3, s[0:1]
	s_waitcnt lgkmcnt(2)
	v_cmp_lt_i32_e64 s[0:1], s11, v6
	s_nop 1
	v_cndmask_b32_e64 v3, 19, v3, s[0:1]
	v_cmp_lt_i32_e64 s[0:1], s11, v7
	s_nop 1
	v_cndmask_b32_e64 v3, 20, v3, s[0:1]
	s_waitcnt lgkmcnt(1)
	v_cmp_lt_i32_e64 s[0:1], s11, v8
	s_nop 1
	v_cndmask_b32_e64 v3, 21, v3, s[0:1]
	v_cmp_lt_i32_e64 s[0:1], s11, v9
	s_nop 1
	v_cndmask_b32_e64 v3, 22, v3, s[0:1]
	s_waitcnt lgkmcnt(0)
	v_cmp_lt_i32_e64 s[0:1], s11, v10
	s_nop 1
	v_cndmask_b32_e64 v3, 23, v3, s[0:1]
	v_cmp_lt_i32_e64 s[0:1], s11, v11
	s_nop 1
	v_cndmask_b32_e64 v3, 24, v3, s[0:1]
	s_add_i32 s0, 0, 0x20464
	v_mov_b32_e32 v4, s0
	ds_read2_b32 v[4:5], v4 offset1:1
	s_add_i32 s0, 0, 0x2046c
	v_mov_b32_e32 v6, s0
	s_add_i32 s0, 0, 0x20474
	v_mov_b32_e32 v8, s0
	s_add_i32 s0, 0, 0x2047c
	v_mov_b32_e32 v10, s0
	ds_read2_b32 v[6:7], v6 offset1:1
	ds_read2_b32 v[8:9], v8 offset1:1
	ds_read_b32 v10, v10
	s_waitcnt lgkmcnt(3)
	v_cmp_lt_i32_e64 s[0:1], s11, v4
	s_nop 1
	v_cndmask_b32_e64 v3, 25, v3, s[0:1]
	v_cmp_lt_i32_e64 s[0:1], s11, v5
	s_nop 1
	v_cndmask_b32_e64 v3, 26, v3, s[0:1]
	s_waitcnt lgkmcnt(2)
	v_cmp_lt_i32_e64 s[0:1], s11, v6
	s_nop 1
	v_cndmask_b32_e64 v3, 27, v3, s[0:1]
	v_cmp_lt_i32_e64 s[0:1], s11, v7
	s_nop 1
	v_cndmask_b32_e64 v3, 28, v3, s[0:1]
	s_waitcnt lgkmcnt(1)
	v_cmp_lt_i32_e64 s[0:1], s11, v8
	s_nop 1
	v_cndmask_b32_e64 v3, 29, v3, s[0:1]
	v_cmp_lt_i32_e64 s[0:1], s11, v9
	s_nop 1
	v_cndmask_b32_e64 v3, 30, v3, s[0:1]
	s_waitcnt lgkmcnt(0)
	v_cmp_lt_i32_e64 s[0:1], s11, v10
	s_nop 1
	v_cndmask_b32_e64 v3, 31, v3, s[0:1]
	s_nop 0
	v_readfirstlane_b32 s0, v3
	s_and_saveexec_b64 s[6:7], vcc
	s_cbranch_execz .LBB0_978
	s_lshl_b32 s1, s0, 2
	s_add_i32 s1, s1, 0
	s_add_i32 s1, s1, 0x20400
	v_mov_b32_e32 v2, s1
	ds_read2_b32 v[2:3], v2 offset1:33
	s_ashr_i32 s1, s0, 31
	s_lshl_b64 s[12:13], s[0:1], 16
	s_waitcnt lgkmcnt(0)
	v_readfirstlane_b32 s0, v2
	s_sub_i32 s0, s11, s0
	s_lshl_b32 s14, s0, 8
	v_subrev_u32_e32 v2, s14, v3
	s_ashr_i32 s15, s14, 31
	v_cmp_gt_i32_e64 s[0:1], v2, v1
	s_add_u32 s11, s8, s12
	s_addc_u32 s12, s9, s13
	v_cndmask_b32_e64 v2, 0, v1, s[0:1]
	s_lshl_b64 s[0:1], s[14:15], 2
	s_add_u32 s0, s11, s0
	v_ashrrev_i32_e32 v3, 31, v2
	s_addc_u32 s1, s12, s1
	v_lshl_add_u64 v[2:3], v[2:3], 2, s[0:1]
	global_load_dword v246, v[2:3], off
	s_bitset1_b32 s99, 2
	s_add_i32 s0, 0, 0x20480
	v_mov_b32_e32 v2, s0
	ds_read_b32 v2, v2
	s_waitcnt lgkmcnt(0)
	v_lshlrev_b32_e32 v2, 3, v2
;     __device__ __forceinline__ const char* bptr(const Unit& u) const { return (const char*)Bt + (size_t)u.pn * 256 * K * 2; }
;     __device__ __forceinline__ unsigned arow(const Unit& u, int r) const { return (unsigned)(u.pm * 256 + r); }
;     __device__ __forceinline__ bool next(int i, Unit& u) const {
;         const int L = i * G + c, total = tb[32] * 8; if (L >= total || i >= 8) return false;
;         const int mt = L >> 3; int e = 0;
;         for (int j = 1; j < 32; ++j) e = (tb[j] <= mt) ? j : e;
;         e = __builtin_amdgcn_readfirstlane(e);
;         u.e = e; u.pm = mt - tb[e]; u.pn = L & 7; u.ui = i;
;         const int rem = tb[33 + e] - u.pm * 256; u.rows = rem < 256 ? rem : 256; return true;
;     }
;     __device__ __forceinline__ const char* bptr(const Unit& u) const { return (const char*)Bt + ((size_t)u.e * 2048 + (size_t)u.pn * 256) * K * 2; }
;     __device__ __forceinline__ unsigned arow(const Unit& u, int r) const { return (unsigned)(rowtab[u.ui * 256 + r] >> a_shift); }
;     __device__ __forceinline__ void fill_rows(const int tid) const {
;         Unit u;
;         for (int i = 0; i < 8 && next(i, u); ++i)
;             if (tid < 256) rowtab[i * 256 + tid] = slot[(size_t)u.e * ECAP + u.pm * 256 + (tid < u.rows ? tid : 0)];
;         __syncthreads();
.LBB0_978:
	s_or_b64 exec, exec, s[6:7]
	s_add_i32 s10, s10, s93
	v_cmp_lt_i32_e64 s[0:1], s10, v2
	s_and_b64 exec, exec, s[0:1]
	s_cbranch_execz .LBB0_993
	s_add_i32 s0, 0, 0x20404
	v_mov_b32_e32 v3, s0
	ds_read2_b32 v[4:5], v3 offset1:1
	s_add_i32 s0, 0, 0x2040c
	v_mov_b32_e32 v3, s0
	s_add_i32 s0, 0, 0x20414
	v_mov_b32_e32 v8, s0
	s_add_i32 s0, 0, 0x2041c
	v_mov_b32_e32 v10, s0
	s_ashr_i32 s11, s10, 3
	ds_read2_b32 v[6:7], v3 offset1:1
	ds_read2_b32 v[8:9], v8 offset1:1
	ds_read2_b32 v[10:11], v10 offset1:1
	s_waitcnt lgkmcnt(3)
	v_cmp_ge_i32_e64 s[0:1], s11, v4
	s_nop 1
	v_cndmask_b32_e64 v3, 0, 1, s[0:1]
	v_cmp_lt_i32_e64 s[0:1], s11, v5
	s_nop 1
	v_cndmask_b32_e64 v3, 2, v3, s[0:1]
	s_waitcnt lgkmcnt(2)
	v_cmp_lt_i32_e64 s[0:1], s11, v6
	s_nop 1
	v_cndmask_b32_e64 v3, 3, v3, s[0:1]
	v_cmp_lt_i32_e64 s[0:1], s11, v7
	s_nop 1
	v_cndmask_b32_e64 v3, 4, v3, s[0:1]
	s_waitcnt lgkmcnt(1)
	v_cmp_lt_i32_e64 s[0:1], s11, v8
	s_nop 1
	v_cndmask_b32_e64 v3, 5, v3, s[0:1]
	v_cmp_lt_i32_e64 s[0:1], s11, v9
	s_nop 1
	v_cndmask_b32_e64 v3, 6, v3, s[0:1]
	s_waitcnt lgkmcnt(0)
	v_cmp_lt_i32_e64 s[0:1], s11, v10
	s_nop 1
	v_cndmask_b32_e64 v3, 7, v3, s[0:1]
	v_cmp_lt_i32_e64 s[0:1], s11, v11
	s_nop 1
	v_cndmask_b32_e64 v3, 8, v3, s[0:1]
	s_add_i32 s0, 0, 0x20424
	v_mov_b32_e32 v4, s0
	ds_read2_b32 v[4:5], v4 offset1:1
	s_add_i32 s0, 0, 0x2042c
	v_mov_b32_e32 v6, s0
	s_add_i32 s0, 0, 0x20434
	v_mov_b32_e32 v8, s0
	s_add_i32 s0, 0, 0x2043c
	v_mov_b32_e32 v10, s0
	ds_read2_b32 v[6:7], v6 offset1:1
	ds_read2_b32 v[8:9], v8 offset1:1
	ds_read2_b32 v[10:11], v10 offset1:1
	s_waitcnt lgkmcnt(3)
	v_cmp_lt_i32_e64 s[0:1], s11, v4
	s_nop 1
	v_cndmask_b32_e64 v3, 9, v3, s[0:1]
	v_cmp_lt_i32_e64 s[0:1], s11, v5
	s_nop 1
	v_cndmask_b32_e64 v3, 10, v3, s[0:1]
	s_waitcnt lgkmcnt(2)
	v_cmp_lt_i32_e64 s[0:1], s11, v6
	s_nop 1
	v_cndmask_b32_e64 v3, 11, v3, s[0:1]
	v_cmp_lt_i32_e64 s[0:1], s11, v7
	s_nop 1
	v_cndmask_b32_e64 v3, 12, v3, s[0:1]
	s_waitcnt lgkmcnt(1)
	v_cmp_lt_i32_e64 s[0:1], s11, v8
	s_nop 1
	v_cndmask_b32_e64 v3, 13, v3, s[0:1]
	v_cmp_lt_i32_e64 s[0:1], s11, v9
	s_nop 1
	v_cndmask_b32_e64 v3, 14, v3, s[0:1]
	s_waitcnt lgkmcnt(0)
	v_cmp_lt_i32_e64 s[0:1], s11, v10
	s_nop 1
	v_cndmask_b32_e64 v3, 15, v3, s[0:1]
	v_cmp_lt_i32_e64 s[0:1], s11, v11
	s_nop 1
	v_cndmask_b32_e64 v3, 16, v3, s[0:1]
	s_add_i32 s0, 0, 0x20444
	v_mov_b32_e32 v4, s0
	ds_read2_b32 v[4:5], v4 offset1:1
	s_add_i32 s0, 0, 0x2044c
	v_mov_b32_e32 v6, s0
	s_add_i32 s0, 0, 0x20454
	v_mov_b32_e32 v8, s0
	s_add_i32 s0, 0, 0x2045c
	v_mov_b32_e32 v10, s0
	ds_read2_b32 v[6:7], v6 offset1:1
	ds_read2_b32 v[8:9], v8 offset1:1
	ds_read2_b32 v[10:11], v10 offset1:1
	s_waitcnt lgkmcnt(3)
	v_cmp_lt_i32_e64 s[0:1], s11, v4
	s_nop 1
	v_cndmask_b32_e64 v3, 17, v3, s[0:1]
	v_cmp_lt_i32_e64 s[0:1], s11, v5
	s_nop 1
	v_cndmask_b32_e64 v3, 18, v3, s[0:1]
	s_waitcnt lgkmcnt(2)
	v_cmp_lt_i32_e64 s[0:1], s11, v6
	s_nop 1
	v_cndmask_b32_e64 v3, 19, v3, s[0:1]
	v_cmp_lt_i32_e64 s[0:1], s11, v7
	s_nop 1
	v_cndmask_b32_e64 v3, 20, v3, s[0:1]
	s_waitcnt lgkmcnt(1)
	v_cmp_lt_i32_e64 s[0:1], s11, v8
	s_nop 1
	v_cndmask_b32_e64 v3, 21, v3, s[0:1]
	v_cmp_lt_i32_e64 s[0:1], s11, v9
	s_nop 1
	v_cndmask_b32_e64 v3, 22, v3, s[0:1]
	s_waitcnt lgkmcnt(0)
	v_cmp_lt_i32_e64 s[0:1], s11, v10
	s_nop 1
	v_cndmask_b32_e64 v3, 23, v3, s[0:1]
	v_cmp_lt_i32_e64 s[0:1], s11, v11
	s_nop 1
	v_cndmask_b32_e64 v3, 24, v3, s[0:1]
	s_add_i32 s0, 0, 0x20464
	v_mov_b32_e32 v4, s0
	ds_read2_b32 v[4:5], v4 offset1:1
	s_add_i32 s0, 0, 0x2046c
	v_mov_b32_e32 v6, s0
	s_add_i32 s0, 0, 0x20474
	v_mov_b32_e32 v8, s0
	s_add_i32 s0, 0, 0x2047c
	v_mov_b32_e32 v10, s0
	ds_read2_b32 v[6:7], v6 offset1:1
	ds_read2_b32 v[8:9], v8 offset1:1
	ds_read_b32 v10, v10
	s_waitcnt lgkmcnt(3)
	v_cmp_lt_i32_e64 s[0:1], s11, v4
	s_nop 1
	v_cndmask_b32_e64 v3, 25, v3, s[0:1]
	v_cmp_lt_i32_e64 s[0:1], s11, v5
	s_nop 1
	v_cndmask_b32_e64 v3, 26, v3, s[0:1]
	s_waitcnt lgkmcnt(2)
	v_cmp_lt_i32_e64 s[0:1], s11, v6
	s_nop 1
	v_cndmask_b32_e64 v3, 27, v3, s[0:1]
	v_cmp_lt_i32_e64 s[0:1], s11, v7
	s_nop 1
	v_cndmask_b32_e64 v3, 28, v3, s[0:1]
	s_waitcnt lgkmcnt(1)
	v_cmp_lt_i32_e64 s[0:1], s11, v8
	s_nop 1
	v_cndmask_b32_e64 v3, 29, v3, s[0:1]
	v_cmp_lt_i32_e64 s[0:1], s11, v9
	s_nop 1
	v_cndmask_b32_e64 v3, 30, v3, s[0:1]
	s_waitcnt lgkmcnt(0)
	v_cmp_lt_i32_e64 s[0:1], s11, v10
	s_nop 1
	v_cndmask_b32_e64 v3, 31, v3, s[0:1]
	s_nop 0
	v_readfirstlane_b32 s0, v3
	s_and_saveexec_b64 s[6:7], vcc
	s_cbranch_execz .LBB0_981
	s_lshl_b32 s1, s0, 2
	s_add_i32 s1, s1, 0
	s_add_i32 s1, s1, 0x20400
	v_mov_b32_e32 v2, s1
	ds_read2_b32 v[2:3], v2 offset1:33
	s_ashr_i32 s1, s0, 31
	s_lshl_b64 s[12:13], s[0:1], 16
	s_waitcnt lgkmcnt(0)
	v_readfirstlane_b32 s0, v2
	s_sub_i32 s0, s11, s0
	s_lshl_b32 s14, s0, 8
	v_subrev_u32_e32 v2, s14, v3
	s_ashr_i32 s15, s14, 31
	v_cmp_gt_i32_e64 s[0:1], v2, v1
	s_add_u32 s11, s8, s12
	s_addc_u32 s12, s9, s13
	v_cndmask_b32_e64 v2, 0, v1, s[0:1]
	s_lshl_b64 s[0:1], s[14:15], 2
	s_add_u32 s0, s11, s0
	v_ashrrev_i32_e32 v3, 31, v2
	s_addc_u32 s1, s12, s1
	v_lshl_add_u64 v[2:3], v[2:3], 2, s[0:1]
	global_load_dword v247, v[2:3], off
	s_bitset1_b32 s99, 3
	s_add_i32 s0, 0, 0x20480
	v_mov_b32_e32 v2, s0
	ds_read_b32 v2, v2
	s_waitcnt lgkmcnt(0)
	v_lshlrev_b32_e32 v2, 3, v2
;     __device__ __forceinline__ const char* bptr(const Unit& u) const { return (const char*)Bt + (size_t)u.pn * 256 * K * 2; }
;     __device__ __forceinline__ unsigned arow(const Unit& u, int r) const { return (unsigned)(u.pm * 256 + r); }
;     __device__ __forceinline__ bool next(int i, Unit& u) const {
;         const int L = i * G + c, total = tb[32] * 8; if (L >= total || i >= 8) return false;
;         const int mt = L >> 3; int e = 0;
;         for (int j = 1; j < 32; ++j) e = (tb[j] <= mt) ? j : e;
;         e = __builtin_amdgcn_readfirstlane(e);
;         u.e = e; u.pm = mt - tb[e]; u.pn = L & 7; u.ui = i;
;         const int rem = tb[33 + e] - u.pm * 256; u.rows = rem < 256 ? rem : 256; return true;
;     }
;     __device__ __forceinline__ const char* bptr(const Unit& u) const { return (const char*)Bt + ((size_t)u.e * 2048 + (size_t)u.pn * 256) * K * 2; }
;     __device__ __forceinline__ unsigned arow(const Unit& u, int r) const { return (unsigned)(rowtab[u.ui * 256 + r] >> a_shift); }
;     __device__ __forceinline__ void fill_rows(const int tid) const {
;         Unit u;
;         for (int i = 0; i < 8 && next(i, u); ++i)
;             if (tid < 256) rowtab[i * 256 + tid] = slot[(size_t)u.e * ECAP + u.pm * 256 + (tid < u.rows ? tid : 0)];
;         __syncthreads();
.LBB0_981:
	s_or_b64 exec, exec, s[6:7]
	s_add_i32 s10, s10, s93
	v_cmp_lt_i32_e64 s[0:1], s10, v2
	s_and_b64 exec, exec, s[0:1]
	s_cbranch_execz .LBB0_993
	s_add_i32 s0, 0, 0x20404
	v_mov_b32_e32 v3, s0
	ds_read2_b32 v[4:5], v3 offset1:1
	s_add_i32 s0, 0, 0x2040c
	v_mov_b32_e32 v3, s0
	s_add_i32 s0, 0, 0x20414
	v_mov_b32_e32 v8, s0
	s_add_i32 s0, 0, 0x2041c
	v_mov_b32_e32 v10, s0
	s_ashr_i32 s11, s10, 3
	ds_read2_b32 v[6:7], v3 offset1:1
	ds_read2_b32 v[8:9], v8 offset1:1
	ds_read2_b32 v[10:11], v10 offset1:1
	s_waitcnt lgkmcnt(3)
	v_cmp_ge_i32_e64 s[0:1], s11, v4
	s_nop 1
	v_cndmask_b32_e64 v3, 0, 1, s[0:1]
	v_cmp_lt_i32_e64 s[0:1], s11, v5
	s_nop 1
	v_cndmask_b32_e64 v3, 2, v3, s[0:1]
	s_waitcnt lgkmcnt(2)
	v_cmp_lt_i32_e64 s[0:1], s11, v6
	s_nop 1
	v_cndmask_b32_e64 v3, 3, v3, s[0:1]
	v_cmp_lt_i32_e64 s[0:1], s11, v7
	s_nop 1
	v_cndmask_b32_e64 v3, 4, v3, s[0:1]
	s_waitcnt lgkmcnt(1)
	v_cmp_lt_i32_e64 s[0:1], s11, v8
	s_nop 1
	v_cndmask_b32_e64 v3, 5, v3, s[0:1]
	v_cmp_lt_i32_e64 s[0:1], s11, v9
	s_nop 1
	v_cndmask_b32_e64 v3, 6, v3, s[0:1]
	s_waitcnt lgkmcnt(0)
	v_cmp_lt_i32_e64 s[0:1], s11, v10
	s_nop 1
	v_cndmask_b32_e64 v3, 7, v3, s[0:1]
	v_cmp_lt_i32_e64 s[0:1], s11, v11
	s_nop 1
	v_cndmask_b32_e64 v3, 8, v3, s[0:1]
	s_add_i32 s0, 0, 0x20424
	v_mov_b32_e32 v4, s0
	ds_read2_b32 v[4:5], v4 offset1:1
	s_add_i32 s0, 0, 0x2042c
	v_mov_b32_e32 v6, s0
	s_add_i32 s0, 0, 0x20434
	v_mov_b32_e32 v8, s0
	s_add_i32 s0, 0, 0x2043c
	v_mov_b32_e32 v10, s0
	ds_read2_b32 v[6:7], v6 offset1:1
	ds_read2_b32 v[8:9], v8 offset1:1
	ds_read2_b32 v[10:11], v10 offset1:1
	s_waitcnt lgkmcnt(3)
	v_cmp_lt_i32_e64 s[0:1], s11, v4
	s_nop 1
	v_cndmask_b32_e64 v3, 9, v3, s[0:1]
	v_cmp_lt_i32_e64 s[0:1], s11, v5
	s_nop 1
	v_cndmask_b32_e64 v3, 10, v3, s[0:1]
	s_waitcnt lgkmcnt(2)
	v_cmp_lt_i32_e64 s[0:1], s11, v6
	s_nop 1
	v_cndmask_b32_e64 v3, 11, v3, s[0:1]
	v_cmp_lt_i32_e64 s[0:1], s11, v7
	s_nop 1
	v_cndmask_b32_e64 v3, 12, v3, s[0:1]
	s_waitcnt lgkmcnt(1)
	v_cmp_lt_i32_e64 s[0:1], s11, v8
	s_nop 1
	v_cndmask_b32_e64 v3, 13, v3, s[0:1]
	v_cmp_lt_i32_e64 s[0:1], s11, v9
	s_nop 1
	v_cndmask_b32_e64 v3, 14, v3, s[0:1]
	s_waitcnt lgkmcnt(0)
	v_cmp_lt_i32_e64 s[0:1], s11, v10
	s_nop 1
	v_cndmask_b32_e64 v3, 15, v3, s[0:1]
	v_cmp_lt_i32_e64 s[0:1], s11, v11
	s_nop 1
	v_cndmask_b32_e64 v3, 16, v3, s[0:1]
	s_add_i32 s0, 0, 0x20444
	v_mov_b32_e32 v4, s0
	ds_read2_b32 v[4:5], v4 offset1:1
	s_add_i32 s0, 0, 0x2044c
	v_mov_b32_e32 v6, s0
	s_add_i32 s0, 0, 0x20454
	v_mov_b32_e32 v8, s0
	s_add_i32 s0, 0, 0x2045c
	v_mov_b32_e32 v10, s0
	ds_read2_b32 v[6:7], v6 offset1:1
	ds_read2_b32 v[8:9], v8 offset1:1
	ds_read2_b32 v[10:11], v10 offset1:1
	s_waitcnt lgkmcnt(3)
	v_cmp_lt_i32_e64 s[0:1], s11, v4
	s_nop 1
	v_cndmask_b32_e64 v3, 17, v3, s[0:1]
	v_cmp_lt_i32_e64 s[0:1], s11, v5
	s_nop 1
	v_cndmask_b32_e64 v3, 18, v3, s[0:1]
	s_waitcnt lgkmcnt(2)
	v_cmp_lt_i32_e64 s[0:1], s11, v6
	s_nop 1
	v_cndmask_b32_e64 v3, 19, v3, s[0:1]
	v_cmp_lt_i32_e64 s[0:1], s11, v7
	s_nop 1
	v_cndmask_b32_e64 v3, 20, v3, s[0:1]
	s_waitcnt lgkmcnt(1)
	v_cmp_lt_i32_e64 s[0:1], s11, v8
	s_nop 1
	v_cndmask_b32_e64 v3, 21, v3, s[0:1]
	v_cmp_lt_i32_e64 s[0:1], s11, v9
	s_nop 1
	v_cndmask_b32_e64 v3, 22, v3, s[0:1]
	s_waitcnt lgkmcnt(0)
	v_cmp_lt_i32_e64 s[0:1], s11, v10
	s_nop 1
	v_cndmask_b32_e64 v3, 23, v3, s[0:1]
	v_cmp_lt_i32_e64 s[0:1], s11, v11
	s_nop 1
	v_cndmask_b32_e64 v3, 24, v3, s[0:1]
	s_add_i32 s0, 0, 0x20464
	v_mov_b32_e32 v4, s0
	ds_read2_b32 v[4:5], v4 offset1:1
	s_add_i32 s0, 0, 0x2046c
	v_mov_b32_e32 v6, s0
	s_add_i32 s0, 0, 0x20474
	v_mov_b32_e32 v8, s0
	s_add_i32 s0, 0, 0x2047c
	v_mov_b32_e32 v10, s0
	ds_read2_b32 v[6:7], v6 offset1:1
	ds_read2_b32 v[8:9], v8 offset1:1
	ds_read_b32 v10, v10
	s_waitcnt lgkmcnt(3)
	v_cmp_lt_i32_e64 s[0:1], s11, v4
	s_nop 1
	v_cndmask_b32_e64 v3, 25, v3, s[0:1]
	v_cmp_lt_i32_e64 s[0:1], s11, v5
	s_nop 1
	v_cndmask_b32_e64 v3, 26, v3, s[0:1]
	s_waitcnt lgkmcnt(2)
	v_cmp_lt_i32_e64 s[0:1], s11, v6
	s_nop 1
	v_cndmask_b32_e64 v3, 27, v3, s[0:1]
	v_cmp_lt_i32_e64 s[0:1], s11, v7
	s_nop 1
	v_cndmask_b32_e64 v3, 28, v3, s[0:1]
	s_waitcnt lgkmcnt(1)
	v_cmp_lt_i32_e64 s[0:1], s11, v8
	s_nop 1
	v_cndmask_b32_e64 v3, 29, v3, s[0:1]
	v_cmp_lt_i32_e64 s[0:1], s11, v9
	s_nop 1
	v_cndmask_b32_e64 v3, 30, v3, s[0:1]
	s_waitcnt lgkmcnt(0)
	v_cmp_lt_i32_e64 s[0:1], s11, v10
	s_nop 1
	v_cndmask_b32_e64 v3, 31, v3, s[0:1]
	s_nop 0
	v_readfirstlane_b32 s0, v3
	s_and_saveexec_b64 s[6:7], vcc
	s_cbranch_execz .LBB0_984
	s_lshl_b32 s1, s0, 2
	s_add_i32 s1, s1, 0
	s_add_i32 s1, s1, 0x20400
	v_mov_b32_e32 v2, s1
	ds_read2_b32 v[2:3], v2 offset1:33
	s_ashr_i32 s1, s0, 31
	s_lshl_b64 s[12:13], s[0:1], 16
	s_waitcnt lgkmcnt(0)
	v_readfirstlane_b32 s0, v2
	s_sub_i32 s0, s11, s0
	s_lshl_b32 s14, s0, 8
	v_subrev_u32_e32 v2, s14, v3
	s_ashr_i32 s15, s14, 31
	v_cmp_gt_i32_e64 s[0:1], v2, v1
	s_add_u32 s11, s8, s12
	s_addc_u32 s12, s9, s13
	v_cndmask_b32_e64 v2, 0, v1, s[0:1]
	s_lshl_b64 s[0:1], s[14:15], 2
	s_add_u32 s0, s11, s0
	v_ashrrev_i32_e32 v3, 31, v2
	s_addc_u32 s1, s12, s1
	v_lshl_add_u64 v[2:3], v[2:3], 2, s[0:1]
	global_load_dword v248, v[2:3], off
	s_bitset1_b32 s99, 4
	s_add_i32 s0, 0, 0x20480
	v_mov_b32_e32 v2, s0
	ds_read_b32 v2, v2
	s_waitcnt lgkmcnt(0)
	v_lshlrev_b32_e32 v2, 3, v2
;     __device__ __forceinline__ const char* bptr(const Unit& u) const { return (const char*)Bt + (size_t)u.pn * 256 * K * 2; }
;     __device__ __forceinline__ unsigned arow(const Unit& u, int r) const { return (unsigned)(u.pm * 256 + r); }
;     __device__ __forceinline__ bool next(int i, Unit& u) const {
;         const int L = i * G + c, total = tb[32] * 8; if (L >= total || i >= 8) return false;
;         const int mt = L >> 3; int e = 0;
;         for (int j = 1; j < 32; ++j) e = (tb[j] <= mt) ? j : e;
;         e = __builtin_amdgcn_readfirstlane(e);
;         u.e = e; u.pm = mt - tb[e]; u.pn = L & 7; u.ui = i;
;         const int rem = tb[33 + e] - u.pm * 256; u.rows = rem < 256 ? rem : 256; return true;
;     }
;     __device__ __forceinline__ const char* bptr(const Unit& u) const { return (const char*)Bt + ((size_t)u.e * 2048 + (size_t)u.pn * 256) * K * 2; }
;     __device__ __forceinline__ unsigned arow(const Unit& u, int r) const { return (unsigned)(rowtab[u.ui * 256 + r] >> a_shift); }
;     __device__ __forceinline__ void fill_rows(const int tid) const {
;         Unit u;
;         for (int i = 0; i < 8 && next(i, u); ++i)
;             if (tid < 256) rowtab[i * 256 + tid] = slot[(size_t)u.e * ECAP + u.pm * 256 + (tid < u.rows ? tid : 0)];
;         __syncthreads();
.LBB0_984:
	s_or_b64 exec, exec, s[6:7]
	s_add_i32 s10, s10, s93
	v_cmp_lt_i32_e64 s[0:1], s10, v2
	s_and_b64 exec, exec, s[0:1]
	s_cbranch_execz .LBB0_993
	s_add_i32 s0, 0, 0x20404
	v_mov_b32_e32 v3, s0
	ds_read2_b32 v[4:5], v3 offset1:1
	s_add_i32 s0, 0, 0x2040c
	v_mov_b32_e32 v3, s0
	s_add_i32 s0, 0, 0x20414
	v_mov_b32_e32 v8, s0
	s_add_i32 s0, 0, 0x2041c
	v_mov_b32_e32 v10, s0
	s_ashr_i32 s11, s10, 3
	ds_read2_b32 v[6:7], v3 offset1:1
	ds_read2_b32 v[8:9], v8 offset1:1
	ds_read2_b32 v[10:11], v10 offset1:1
	s_waitcnt lgkmcnt(3)
	v_cmp_ge_i32_e64 s[0:1], s11, v4
	s_nop 1
	v_cndmask_b32_e64 v3, 0, 1, s[0:1]
	v_cmp_lt_i32_e64 s[0:1], s11, v5
	s_nop 1
	v_cndmask_b32_e64 v3, 2, v3, s[0:1]
	s_waitcnt lgkmcnt(2)
	v_cmp_lt_i32_e64 s[0:1], s11, v6
	s_nop 1
	v_cndmask_b32_e64 v3, 3, v3, s[0:1]
	v_cmp_lt_i32_e64 s[0:1], s11, v7
	s_nop 1
	v_cndmask_b32_e64 v3, 4, v3, s[0:1]
	s_waitcnt lgkmcnt(1)
	v_cmp_lt_i32_e64 s[0:1], s11, v8
	s_nop 1
	v_cndmask_b32_e64 v3, 5, v3, s[0:1]
	v_cmp_lt_i32_e64 s[0:1], s11, v9
	s_nop 1
	v_cndmask_b32_e64 v3, 6, v3, s[0:1]
	s_waitcnt lgkmcnt(0)
	v_cmp_lt_i32_e64 s[0:1], s11, v10
	s_nop 1
	v_cndmask_b32_e64 v3, 7, v3, s[0:1]
	v_cmp_lt_i32_e64 s[0:1], s11, v11
	s_nop 1
	v_cndmask_b32_e64 v3, 8, v3, s[0:1]
	s_add_i32 s0, 0, 0x20424
	v_mov_b32_e32 v4, s0
	ds_read2_b32 v[4:5], v4 offset1:1
	s_add_i32 s0, 0, 0x2042c
	v_mov_b32_e32 v6, s0
	s_add_i32 s0, 0, 0x20434
	v_mov_b32_e32 v8, s0
	s_add_i32 s0, 0, 0x2043c
	v_mov_b32_e32 v10, s0
	ds_read2_b32 v[6:7], v6 offset1:1
	ds_read2_b32 v[8:9], v8 offset1:1
	ds_read2_b32 v[10:11], v10 offset1:1
	s_waitcnt lgkmcnt(3)
	v_cmp_lt_i32_e64 s[0:1], s11, v4
	s_nop 1
	v_cndmask_b32_e64 v3, 9, v3, s[0:1]
	v_cmp_lt_i32_e64 s[0:1], s11, v5
	s_nop 1
	v_cndmask_b32_e64 v3, 10, v3, s[0:1]
	s_waitcnt lgkmcnt(2)
	v_cmp_lt_i32_e64 s[0:1], s11, v6
	s_nop 1
	v_cndmask_b32_e64 v3, 11, v3, s[0:1]
	v_cmp_lt_i32_e64 s[0:1], s11, v7
	s_nop 1
	v_cndmask_b32_e64 v3, 12, v3, s[0:1]
	s_waitcnt lgkmcnt(1)
	v_cmp_lt_i32_e64 s[0:1], s11, v8
	s_nop 1
	v_cndmask_b32_e64 v3, 13, v3, s[0:1]
	v_cmp_lt_i32_e64 s[0:1], s11, v9
	s_nop 1
	v_cndmask_b32_e64 v3, 14, v3, s[0:1]
	s_waitcnt lgkmcnt(0)
	v_cmp_lt_i32_e64 s[0:1], s11, v10
	s_nop 1
	v_cndmask_b32_e64 v3, 15, v3, s[0:1]
	v_cmp_lt_i32_e64 s[0:1], s11, v11
	s_nop 1
	v_cndmask_b32_e64 v3, 16, v3, s[0:1]
	s_add_i32 s0, 0, 0x20444
	v_mov_b32_e32 v4, s0
	ds_read2_b32 v[4:5], v4 offset1:1
	s_add_i32 s0, 0, 0x2044c
	v_mov_b32_e32 v6, s0
	s_add_i32 s0, 0, 0x20454
	v_mov_b32_e32 v8, s0
	s_add_i32 s0, 0, 0x2045c
	v_mov_b32_e32 v10, s0
	ds_read2_b32 v[6:7], v6 offset1:1
	ds_read2_b32 v[8:9], v8 offset1:1
	ds_read2_b32 v[10:11], v10 offset1:1
	s_waitcnt lgkmcnt(3)
	v_cmp_lt_i32_e64 s[0:1], s11, v4
	s_nop 1
	v_cndmask_b32_e64 v3, 17, v3, s[0:1]
	v_cmp_lt_i32_e64 s[0:1], s11, v5
	s_nop 1
	v_cndmask_b32_e64 v3, 18, v3, s[0:1]
	s_waitcnt lgkmcnt(2)
	v_cmp_lt_i32_e64 s[0:1], s11, v6
	s_nop 1
	v_cndmask_b32_e64 v3, 19, v3, s[0:1]
	v_cmp_lt_i32_e64 s[0:1], s11, v7
	s_nop 1
	v_cndmask_b32_e64 v3, 20, v3, s[0:1]
	s_waitcnt lgkmcnt(1)
	v_cmp_lt_i32_e64 s[0:1], s11, v8
	s_nop 1
	v_cndmask_b32_e64 v3, 21, v3, s[0:1]
	v_cmp_lt_i32_e64 s[0:1], s11, v9
	s_nop 1
	v_cndmask_b32_e64 v3, 22, v3, s[0:1]
	s_waitcnt lgkmcnt(0)
	v_cmp_lt_i32_e64 s[0:1], s11, v10
	s_nop 1
	v_cndmask_b32_e64 v3, 23, v3, s[0:1]
	v_cmp_lt_i32_e64 s[0:1], s11, v11
	s_nop 1
	v_cndmask_b32_e64 v3, 24, v3, s[0:1]
	s_add_i32 s0, 0, 0x20464
	v_mov_b32_e32 v4, s0
	ds_read2_b32 v[4:5], v4 offset1:1
	s_add_i32 s0, 0, 0x2046c
	v_mov_b32_e32 v6, s0
	s_add_i32 s0, 0, 0x20474
	v_mov_b32_e32 v8, s0
	s_add_i32 s0, 0, 0x2047c
	v_mov_b32_e32 v10, s0
	ds_read2_b32 v[6:7], v6 offset1:1
	ds_read2_b32 v[8:9], v8 offset1:1
	ds_read_b32 v10, v10
	s_waitcnt lgkmcnt(3)
	v_cmp_lt_i32_e64 s[0:1], s11, v4
	s_nop 1
	v_cndmask_b32_e64 v3, 25, v3, s[0:1]
	v_cmp_lt_i32_e64 s[0:1], s11, v5
	s_nop 1
	v_cndmask_b32_e64 v3, 26, v3, s[0:1]
	s_waitcnt lgkmcnt(2)
	v_cmp_lt_i32_e64 s[0:1], s11, v6
	s_nop 1
	v_cndmask_b32_e64 v3, 27, v3, s[0:1]
	v_cmp_lt_i32_e64 s[0:1], s11, v7
	s_nop 1
	v_cndmask_b32_e64 v3, 28, v3, s[0:1]
	s_waitcnt lgkmcnt(1)
	v_cmp_lt_i32_e64 s[0:1], s11, v8
	s_nop 1
	v_cndmask_b32_e64 v3, 29, v3, s[0:1]
	v_cmp_lt_i32_e64 s[0:1], s11, v9
	s_nop 1
	v_cndmask_b32_e64 v3, 30, v3, s[0:1]
	s_waitcnt lgkmcnt(0)
	v_cmp_lt_i32_e64 s[0:1], s11, v10
	s_nop 1
	v_cndmask_b32_e64 v3, 31, v3, s[0:1]
	s_nop 0
	v_readfirstlane_b32 s0, v3
	s_and_saveexec_b64 s[6:7], vcc
	s_cbranch_execz .LBB0_987
	s_lshl_b32 s1, s0, 2
	s_add_i32 s1, s1, 0
	s_add_i32 s1, s1, 0x20400
	v_mov_b32_e32 v2, s1
	ds_read2_b32 v[2:3], v2 offset1:33
	s_ashr_i32 s1, s0, 31
	s_lshl_b64 s[12:13], s[0:1], 16
	s_waitcnt lgkmcnt(0)
	v_readfirstlane_b32 s0, v2
	s_sub_i32 s0, s11, s0
	s_lshl_b32 s14, s0, 8
	v_subrev_u32_e32 v2, s14, v3
	s_ashr_i32 s15, s14, 31
	v_cmp_gt_i32_e64 s[0:1], v2, v1
	s_add_u32 s11, s8, s12
	s_addc_u32 s12, s9, s13
	v_cndmask_b32_e64 v2, 0, v1, s[0:1]
	s_lshl_b64 s[0:1], s[14:15], 2
	s_add_u32 s0, s11, s0
	v_ashrrev_i32_e32 v3, 31, v2
	s_addc_u32 s1, s12, s1
	v_lshl_add_u64 v[2:3], v[2:3], 2, s[0:1]
	global_load_dword v249, v[2:3], off
	s_bitset1_b32 s99, 5
	s_add_i32 s0, 0, 0x20480
	v_mov_b32_e32 v2, s0
	ds_read_b32 v2, v2
	s_waitcnt lgkmcnt(0)
	v_lshlrev_b32_e32 v2, 3, v2
;     __device__ __forceinline__ const char* bptr(const Unit& u) const { return (const char*)Bt + (size_t)u.pn * 256 * K * 2; }
;     __device__ __forceinline__ unsigned arow(const Unit& u, int r) const { return (unsigned)(u.pm * 256 + r); }
;     __device__ __forceinline__ bool next(int i, Unit& u) const {
;         const int L = i * G + c, total = tb[32] * 8; if (L >= total || i >= 8) return false;
;         const int mt = L >> 3; int e = 0;
;         for (int j = 1; j < 32; ++j) e = (tb[j] <= mt) ? j : e;
;         e = __builtin_amdgcn_readfirstlane(e);
;         u.e = e; u.pm = mt - tb[e]; u.pn = L & 7; u.ui = i;
;         const int rem = tb[33 + e] - u.pm * 256; u.rows = rem < 256 ? rem : 256; return true;
;     }
;     __device__ __forceinline__ const char* bptr(const Unit& u) const { return (const char*)Bt + ((size_t)u.e * 2048 + (size_t)u.pn * 256) * K * 2; }
;     __device__ __forceinline__ unsigned arow(const Unit& u, int r) const { return (unsigned)(rowtab[u.ui * 256 + r] >> a_shift); }
;     __device__ __forceinline__ void fill_rows(const int tid) const {
;         Unit u;
;         for (int i = 0; i < 8 && next(i, u); ++i)
;             if (tid < 256) rowtab[i * 256 + tid] = slot[(size_t)u.e * ECAP + u.pm * 256 + (tid < u.rows ? tid : 0)];
;         __syncthreads();
.LBB0_987:
	s_or_b64 exec, exec, s[6:7]
	s_add_i32 s10, s10, s93
	v_cmp_lt_i32_e64 s[0:1], s10, v2
	s_and_b64 exec, exec, s[0:1]
	s_cbranch_execz .LBB0_993
	s_add_i32 s0, 0, 0x20404
	v_mov_b32_e32 v3, s0
	ds_read2_b32 v[4:5], v3 offset1:1
	s_add_i32 s0, 0, 0x2040c
	v_mov_b32_e32 v3, s0
	s_add_i32 s0, 0, 0x20414
	v_mov_b32_e32 v8, s0
	s_add_i32 s0, 0, 0x2041c
	v_mov_b32_e32 v10, s0
	s_ashr_i32 s11, s10, 3
	ds_read2_b32 v[6:7], v3 offset1:1
	ds_read2_b32 v[8:9], v8 offset1:1
	ds_read2_b32 v[10:11], v10 offset1:1
	s_waitcnt lgkmcnt(3)
	v_cmp_ge_i32_e64 s[0:1], s11, v4
	s_nop 1
	v_cndmask_b32_e64 v3, 0, 1, s[0:1]
	v_cmp_lt_i32_e64 s[0:1], s11, v5
	s_nop 1
	v_cndmask_b32_e64 v3, 2, v3, s[0:1]
	s_waitcnt lgkmcnt(2)
	v_cmp_lt_i32_e64 s[0:1], s11, v6
	s_nop 1
	v_cndmask_b32_e64 v3, 3, v3, s[0:1]
	v_cmp_lt_i32_e64 s[0:1], s11, v7
	s_nop 1
	v_cndmask_b32_e64 v3, 4, v3, s[0:1]
	s_waitcnt lgkmcnt(1)
	v_cmp_lt_i32_e64 s[0:1], s11, v8
	s_nop 1
	v_cndmask_b32_e64 v3, 5, v3, s[0:1]
	v_cmp_lt_i32_e64 s[0:1], s11, v9
	s_nop 1
	v_cndmask_b32_e64 v3, 6, v3, s[0:1]
	s_waitcnt lgkmcnt(0)
	v_cmp_lt_i32_e64 s[0:1], s11, v10
	s_nop 1
	v_cndmask_b32_e64 v3, 7, v3, s[0:1]
	v_cmp_lt_i32_e64 s[0:1], s11, v11
	s_nop 1
	v_cndmask_b32_e64 v3, 8, v3, s[0:1]
	s_add_i32 s0, 0, 0x20424
	v_mov_b32_e32 v4, s0
	ds_read2_b32 v[4:5], v4 offset1:1
	s_add_i32 s0, 0, 0x2042c
	v_mov_b32_e32 v6, s0
	s_add_i32 s0, 0, 0x20434
	v_mov_b32_e32 v8, s0
	s_add_i32 s0, 0, 0x2043c
	v_mov_b32_e32 v10, s0
	ds_read2_b32 v[6:7], v6 offset1:1
	ds_read2_b32 v[8:9], v8 offset1:1
	ds_read2_b32 v[10:11], v10 offset1:1
	s_waitcnt lgkmcnt(3)
	v_cmp_lt_i32_e64 s[0:1], s11, v4
	s_nop 1
	v_cndmask_b32_e64 v3, 9, v3, s[0:1]
	v_cmp_lt_i32_e64 s[0:1], s11, v5
	s_nop 1
	v_cndmask_b32_e64 v3, 10, v3, s[0:1]
	s_waitcnt lgkmcnt(2)
	v_cmp_lt_i32_e64 s[0:1], s11, v6
	s_nop 1
	v_cndmask_b32_e64 v3, 11, v3, s[0:1]
	v_cmp_lt_i32_e64 s[0:1], s11, v7
	s_nop 1
	v_cndmask_b32_e64 v3, 12, v3, s[0:1]
	s_waitcnt lgkmcnt(1)
	v_cmp_lt_i32_e64 s[0:1], s11, v8
	s_nop 1
	v_cndmask_b32_e64 v3, 13, v3, s[0:1]
	v_cmp_lt_i32_e64 s[0:1], s11, v9
	s_nop 1
	v_cndmask_b32_e64 v3, 14, v3, s[0:1]
	s_waitcnt lgkmcnt(0)
	v_cmp_lt_i32_e64 s[0:1], s11, v10
	s_nop 1
	v_cndmask_b32_e64 v3, 15, v3, s[0:1]
	v_cmp_lt_i32_e64 s[0:1], s11, v11
	s_nop 1
	v_cndmask_b32_e64 v3, 16, v3, s[0:1]
	s_add_i32 s0, 0, 0x20444
	v_mov_b32_e32 v4, s0
	ds_read2_b32 v[4:5], v4 offset1:1
	s_add_i32 s0, 0, 0x2044c
	v_mov_b32_e32 v6, s0
	s_add_i32 s0, 0, 0x20454
	v_mov_b32_e32 v8, s0
	s_add_i32 s0, 0, 0x2045c
	v_mov_b32_e32 v10, s0
	ds_read2_b32 v[6:7], v6 offset1:1
	ds_read2_b32 v[8:9], v8 offset1:1
	ds_read2_b32 v[10:11], v10 offset1:1
	s_waitcnt lgkmcnt(3)
	v_cmp_lt_i32_e64 s[0:1], s11, v4
	s_nop 1
	v_cndmask_b32_e64 v3, 17, v3, s[0:1]
	v_cmp_lt_i32_e64 s[0:1], s11, v5
	s_nop 1
	v_cndmask_b32_e64 v3, 18, v3, s[0:1]
	s_waitcnt lgkmcnt(2)
	v_cmp_lt_i32_e64 s[0:1], s11, v6
	s_nop 1
	v_cndmask_b32_e64 v3, 19, v3, s[0:1]
	v_cmp_lt_i32_e64 s[0:1], s11, v7
	s_nop 1
	v_cndmask_b32_e64 v3, 20, v3, s[0:1]
	s_waitcnt lgkmcnt(1)
	v_cmp_lt_i32_e64 s[0:1], s11, v8
	s_nop 1
	v_cndmask_b32_e64 v3, 21, v3, s[0:1]
	v_cmp_lt_i32_e64 s[0:1], s11, v9
	s_nop 1
	v_cndmask_b32_e64 v3, 22, v3, s[0:1]
	s_waitcnt lgkmcnt(0)
	v_cmp_lt_i32_e64 s[0:1], s11, v10
	s_nop 1
	v_cndmask_b32_e64 v3, 23, v3, s[0:1]
	v_cmp_lt_i32_e64 s[0:1], s11, v11
	s_nop 1
	v_cndmask_b32_e64 v3, 24, v3, s[0:1]
	s_add_i32 s0, 0, 0x20464
	v_mov_b32_e32 v4, s0
	ds_read2_b32 v[4:5], v4 offset1:1
	s_add_i32 s0, 0, 0x2046c
	v_mov_b32_e32 v6, s0
	s_add_i32 s0, 0, 0x20474
	v_mov_b32_e32 v8, s0
	s_add_i32 s0, 0, 0x2047c
	v_mov_b32_e32 v10, s0
	ds_read2_b32 v[6:7], v6 offset1:1
	ds_read2_b32 v[8:9], v8 offset1:1
	ds_read_b32 v10, v10
	s_waitcnt lgkmcnt(3)
	v_cmp_lt_i32_e64 s[0:1], s11, v4
	s_nop 1
	v_cndmask_b32_e64 v3, 25, v3, s[0:1]
	v_cmp_lt_i32_e64 s[0:1], s11, v5
	s_nop 1
	v_cndmask_b32_e64 v3, 26, v3, s[0:1]
	s_waitcnt lgkmcnt(2)
	v_cmp_lt_i32_e64 s[0:1], s11, v6
	s_nop 1
	v_cndmask_b32_e64 v3, 27, v3, s[0:1]
	v_cmp_lt_i32_e64 s[0:1], s11, v7
	s_nop 1
	v_cndmask_b32_e64 v3, 28, v3, s[0:1]
	s_waitcnt lgkmcnt(1)
	v_cmp_lt_i32_e64 s[0:1], s11, v8
	s_nop 1
	v_cndmask_b32_e64 v3, 29, v3, s[0:1]
	v_cmp_lt_i32_e64 s[0:1], s11, v9
	s_nop 1
	v_cndmask_b32_e64 v3, 30, v3, s[0:1]
	s_waitcnt lgkmcnt(0)
	v_cmp_lt_i32_e64 s[0:1], s11, v10
	s_nop 1
	v_cndmask_b32_e64 v3, 31, v3, s[0:1]
	s_nop 0
	v_readfirstlane_b32 s0, v3
	s_and_saveexec_b64 s[6:7], vcc
	s_cbranch_execz .LBB0_990
	s_lshl_b32 s1, s0, 2
	s_add_i32 s1, s1, 0
	s_add_i32 s1, s1, 0x20400
	v_mov_b32_e32 v2, s1
	ds_read2_b32 v[2:3], v2 offset1:33
	s_ashr_i32 s1, s0, 31
	s_lshl_b64 s[12:13], s[0:1], 16
	s_waitcnt lgkmcnt(0)
	v_readfirstlane_b32 s0, v2
	s_sub_i32 s0, s11, s0
	s_lshl_b32 s14, s0, 8
	v_subrev_u32_e32 v2, s14, v3
	s_ashr_i32 s15, s14, 31
	v_cmp_gt_i32_e64 s[0:1], v2, v1
	s_add_u32 s11, s8, s12
	s_addc_u32 s12, s9, s13
	v_cndmask_b32_e64 v2, 0, v1, s[0:1]
	s_lshl_b64 s[0:1], s[14:15], 2
	s_add_u32 s0, s11, s0
	v_ashrrev_i32_e32 v3, 31, v2
	s_addc_u32 s1, s12, s1
	v_lshl_add_u64 v[2:3], v[2:3], 2, s[0:1]
	global_load_dword v250, v[2:3], off
	s_bitset1_b32 s99, 6
	s_add_i32 s0, 0, 0x20480
	v_mov_b32_e32 v2, s0
	ds_read_b32 v2, v2
	s_waitcnt lgkmcnt(0)
	v_lshlrev_b32_e32 v2, 3, v2
;     __device__ __forceinline__ const char* bptr(const Unit& u) const { return (const char*)Bt + (size_t)u.pn * 256 * K * 2; }
;     __device__ __forceinline__ unsigned arow(const Unit& u, int r) const { return (unsigned)(u.pm * 256 + r); }
;     __device__ __forceinline__ bool next(int i, Unit& u) const {
;         const int L = i * G + c, total = tb[32] * 8; if (L >= total || i >= 8) return false;
;         const int mt = L >> 3; int e = 0;
;         for (int j = 1; j < 32; ++j) e = (tb[j] <= mt) ? j : e;
;         e = __builtin_amdgcn_readfirstlane(e);
;         u.e = e; u.pm = mt - tb[e]; u.pn = L & 7; u.ui = i;
;         const int rem = tb[33 + e] - u.pm * 256; u.rows = rem < 256 ? rem : 256; return true;
;     }
;     __device__ __forceinline__ const char* bptr(const Unit& u) const { return (const char*)Bt + ((size_t)u.e * 2048 + (size_t)u.pn * 256) * K * 2; }
;     __device__ __forceinline__ unsigned arow(const Unit& u, int r) const { return (unsigned)(rowtab[u.ui * 256 + r] >> a_shift); }
;     __device__ __forceinline__ void fill_rows(const int tid) const {
;         Unit u;
;         for (int i = 0; i < 8 && next(i, u); ++i)
;             if (tid < 256) rowtab[i * 256 + tid] = slot[(size_t)u.e * ECAP + u.pm * 256 + (tid < u.rows ? tid : 0)];
;         __syncthreads();
.LBB0_990:
	s_or_b64 exec, exec, s[6:7]
	s_add_i32 s10, s10, s93
	v_cmp_lt_i32_e64 s[0:1], s10, v2
	s_and_b64 exec, exec, s[0:1]
	s_cbranch_execz .LBB0_993
	s_add_i32 s0, 0, 0x20404
	v_mov_b32_e32 v2, s0
	ds_read2_b32 v[2:3], v2 offset1:1
	s_add_i32 s0, 0, 0x2040c
	v_mov_b32_e32 v4, s0
	s_add_i32 s0, 0, 0x20414
	v_mov_b32_e32 v6, s0
	s_add_i32 s0, 0, 0x2041c
	v_mov_b32_e32 v8, s0
	s_ashr_i32 s6, s10, 3
	ds_read2_b32 v[4:5], v4 offset1:1
	ds_read2_b32 v[6:7], v6 offset1:1
	ds_read2_b32 v[8:9], v8 offset1:1
	s_waitcnt lgkmcnt(3)
	v_cmp_ge_i32_e64 s[0:1], s6, v2
	s_nop 1
	v_cndmask_b32_e64 v2, 0, 1, s[0:1]
	v_cmp_lt_i32_e64 s[0:1], s6, v3
	s_nop 1
	v_cndmask_b32_e64 v2, 2, v2, s[0:1]
	s_waitcnt lgkmcnt(2)
	v_cmp_lt_i32_e64 s[0:1], s6, v4
	s_nop 1
	v_cndmask_b32_e64 v2, 3, v2, s[0:1]
	v_cmp_lt_i32_e64 s[0:1], s6, v5
	s_nop 1
	v_cndmask_b32_e64 v2, 4, v2, s[0:1]
	s_waitcnt lgkmcnt(1)
	v_cmp_lt_i32_e64 s[0:1], s6, v6
	s_nop 1
	v_cndmask_b32_e64 v2, 5, v2, s[0:1]
	v_cmp_lt_i32_e64 s[0:1], s6, v7
	s_nop 1
	v_cndmask_b32_e64 v2, 6, v2, s[0:1]
	s_waitcnt lgkmcnt(0)
	v_cmp_lt_i32_e64 s[0:1], s6, v8
	s_nop 1
	v_cndmask_b32_e64 v2, 7, v2, s[0:1]
	v_cmp_lt_i32_e64 s[0:1], s6, v9
	s_nop 1
	v_cndmask_b32_e64 v10, 8, v2, s[0:1]
	s_add_i32 s0, 0, 0x20424
	v_mov_b32_e32 v2, s0
	ds_read2_b32 v[2:3], v2 offset1:1
	s_add_i32 s0, 0, 0x2042c
	v_mov_b32_e32 v4, s0
	s_add_i32 s0, 0, 0x20434
	v_mov_b32_e32 v6, s0
	s_add_i32 s0, 0, 0x2043c
	v_mov_b32_e32 v8, s0
	ds_read2_b32 v[4:5], v4 offset1:1
	ds_read2_b32 v[6:7], v6 offset1:1
	ds_read2_b32 v[8:9], v8 offset1:1
	s_waitcnt lgkmcnt(3)
	v_cmp_lt_i32_e64 s[0:1], s6, v2
	s_nop 1
	v_cndmask_b32_e64 v2, 9, v10, s[0:1]
	v_cmp_lt_i32_e64 s[0:1], s6, v3
	s_nop 1
	v_cndmask_b32_e64 v2, 10, v2, s[0:1]
	s_waitcnt lgkmcnt(2)
	v_cmp_lt_i32_e64 s[0:1], s6, v4
	s_nop 1
	v_cndmask_b32_e64 v2, 11, v2, s[0:1]
	v_cmp_lt_i32_e64 s[0:1], s6, v5
	s_nop 1
	v_cndmask_b32_e64 v2, 12, v2, s[0:1]
	s_waitcnt lgkmcnt(1)
	v_cmp_lt_i32_e64 s[0:1], s6, v6
	s_nop 1
	v_cndmask_b32_e64 v2, 13, v2, s[0:1]
	v_cmp_lt_i32_e64 s[0:1], s6, v7
	s_nop 1
	v_cndmask_b32_e64 v2, 14, v2, s[0:1]
	s_waitcnt lgkmcnt(0)
	v_cmp_lt_i32_e64 s[0:1], s6, v8
	s_nop 1
	v_cndmask_b32_e64 v2, 15, v2, s[0:1]
	v_cmp_lt_i32_e64 s[0:1], s6, v9
	s_nop 1
	v_cndmask_b32_e64 v10, 16, v2, s[0:1]
	s_add_i32 s0, 0, 0x20444
	v_mov_b32_e32 v2, s0
	ds_read2_b32 v[2:3], v2 offset1:1
	s_add_i32 s0, 0, 0x2044c
	v_mov_b32_e32 v4, s0
	s_add_i32 s0, 0, 0x20454
	v_mov_b32_e32 v6, s0
	s_add_i32 s0, 0, 0x2045c
	v_mov_b32_e32 v8, s0
	ds_read2_b32 v[4:5], v4 offset1:1
	ds_read2_b32 v[6:7], v6 offset1:1
	ds_read2_b32 v[8:9], v8 offset1:1
	s_waitcnt lgkmcnt(3)
	v_cmp_lt_i32_e64 s[0:1], s6, v2
	s_nop 1
	v_cndmask_b32_e64 v2, 17, v10, s[0:1]
	v_cmp_lt_i32_e64 s[0:1], s6, v3
	s_nop 1
	v_cndmask_b32_e64 v2, 18, v2, s[0:1]
	s_waitcnt lgkmcnt(2)
	v_cmp_lt_i32_e64 s[0:1], s6, v4
	s_nop 1
	v_cndmask_b32_e64 v2, 19, v2, s[0:1]
	v_cmp_lt_i32_e64 s[0:1], s6, v5
	s_nop 1
	v_cndmask_b32_e64 v2, 20, v2, s[0:1]
	s_waitcnt lgkmcnt(1)
	v_cmp_lt_i32_e64 s[0:1], s6, v6
	s_nop 1
	v_cndmask_b32_e64 v2, 21, v2, s[0:1]
	v_cmp_lt_i32_e64 s[0:1], s6, v7
	s_nop 1
	v_cndmask_b32_e64 v2, 22, v2, s[0:1]
	s_waitcnt lgkmcnt(0)
	v_cmp_lt_i32_e64 s[0:1], s6, v8
	s_nop 1
	v_cndmask_b32_e64 v2, 23, v2, s[0:1]
	v_cmp_lt_i32_e64 s[0:1], s6, v9
	s_nop 1
	v_cndmask_b32_e64 v8, 24, v2, s[0:1]
	s_add_i32 s0, 0, 0x20464
	v_mov_b32_e32 v2, s0
	ds_read2_b32 v[2:3], v2 offset1:1
	s_add_i32 s0, 0, 0x2046c
	v_mov_b32_e32 v4, s0
	s_add_i32 s0, 0, 0x20474
	v_mov_b32_e32 v6, s0
	s_add_i32 s0, 0, 0x2047c
	v_mov_b32_e32 v9, s0
	ds_read2_b32 v[4:5], v4 offset1:1
	ds_read2_b32 v[6:7], v6 offset1:1
	ds_read_b32 v9, v9
	s_waitcnt lgkmcnt(3)
	v_cmp_lt_i32_e64 s[0:1], s6, v2
	s_nop 1
	v_cndmask_b32_e64 v2, 25, v8, s[0:1]
	v_cmp_lt_i32_e64 s[0:1], s6, v3
	s_nop 1
	v_cndmask_b32_e64 v2, 26, v2, s[0:1]
	s_waitcnt lgkmcnt(2)
	v_cmp_lt_i32_e64 s[0:1], s6, v4
	s_nop 1
	v_cndmask_b32_e64 v2, 27, v2, s[0:1]
	v_cmp_lt_i32_e64 s[0:1], s6, v5
	s_nop 1
	v_cndmask_b32_e64 v2, 28, v2, s[0:1]
	s_waitcnt lgkmcnt(1)
	v_cmp_lt_i32_e64 s[0:1], s6, v6
	s_nop 1
	v_cndmask_b32_e64 v2, 29, v2, s[0:1]
	v_cmp_lt_i32_e64 s[0:1], s6, v7
	s_nop 1
	v_cndmask_b32_e64 v2, 30, v2, s[0:1]
	s_waitcnt lgkmcnt(0)
	v_cmp_lt_i32_e64 s[0:1], s6, v9
	s_nop 1
	v_cndmask_b32_e64 v2, 31, v2, s[0:1]
	s_nop 0
	v_readfirstlane_b32 s0, v2
	s_and_b64 exec, exec, vcc
	s_cbranch_execz .LBB0_993
	s_lshl_b32 s1, s0, 2
	s_add_i32 s1, s1, 0
	s_add_i32 s1, s1, 0x20400
	v_mov_b32_e32 v2, s1
	ds_read2_b32 v[2:3], v2 offset1:33
	s_ashr_i32 s1, s0, 31
	s_lshl_b64 s[0:1], s[0:1], 16
	s_waitcnt lgkmcnt(0)
	v_readfirstlane_b32 s7, v2
	s_sub_i32 s6, s6, s7
	s_lshl_b32 s6, s6, 8
	s_ashr_i32 s7, s6, 31
	v_subrev_u32_e32 v2, s6, v3
	s_add_u32 s8, s8, s0
	v_cmp_gt_i32_e32 vcc, v2, v1
	s_addc_u32 s9, s9, s1
	s_lshl_b64 s[0:1], s[6:7], 2
	v_cndmask_b32_e32 v2, 0, v1, vcc
	s_add_u32 s0, s8, s0
	v_ashrrev_i32_e32 v3, 31, v2
	s_addc_u32 s1, s9, s1
	v_lshl_add_u64 v[2:3], v[2:3], 2, s[0:1]
	global_load_dword v251, v[2:3], off
	s_bitset1_b32 s99, 7

;     __device__ __forceinline__ void fill_rows(const int tid) const {
;     ...
;             if (tid < 256) rowtab[i * 256 + tid] = slot[(size_t)u.e * ECAP + u.pm * 256 + (tid < u.rows ? tid : 0)];
;         __syncthreads();
.LBB0_994:
	s_cmp_eq_u32 s99, 0
	s_cbranch_scc1 .Lmy_fr_0
	s_waitcnt vmcnt(0)
	ds_write_b32 v0, v244
	s_bitcmp1_b32 s99, 1
	s_cbranch_scc0 .Lmy_fr_0
	ds_write_b32 v0, v245 offset:1024
	s_bitcmp1_b32 s99, 2
	s_cbranch_scc0 .Lmy_fr_0
	ds_write_b32 v0, v246 offset:2048
	s_bitcmp1_b32 s99, 3
	s_cbranch_scc0 .Lmy_fr_0
	ds_write_b32 v0, v247 offset:3072
	s_bitcmp1_b32 s99, 4
	s_cbranch_scc0 .Lmy_fr_0
	ds_write_b32 v0, v248 offset:4096
	s_bitcmp1_b32 s99, 5
	s_cbranch_scc0 .Lmy_fr_0
	ds_write_b32 v0, v249 offset:5120
	s_bitcmp1_b32 s99, 6
	s_cbranch_scc0 .Lmy_fr_0
	ds_write_b32 v0, v250 offset:6144
	s_bitcmp1_b32 s99, 7
	s_cbranch_scc0 .Lmy_fr_0
	ds_write_b32 v0, v251 offset:7168

; #define LAS __attribute__((address_space(3)))
; __device__ __forceinline__ int mk_tid(const int wv) { int ln; asm volatile("v_mbcnt_lo_u32_b32 %0, -1, 0\n\tv_mbcnt_hi_u32_b32 %0, -1, %0" : "=v"(ln)); return wv * 64 + ln; }
; __device__ __forceinline__ void moe_tiles(const int* cnt, LAS int* tb, const int wv) {
;     if (mk_tid(wv) == 0) { int acc = 0; for (int e = 0; e < 32; ++e) { const int c = cnt[e]; tb[e] = acc; tb[33 + e] = c; acc += (c + 255) >> 8; } tb[32] = acc; }
;     __syncthreads();
; }
.LBB0_1128:
	s_cmp_lt_i32 s78, 8
	s_cselect_b64 s[4:5], -1, 0
	s_and_b64 s[0:1], s[4:5], s[0:1]
	s_andn2_b64 vcc, exec, s[0:1]
	s_cbranch_vccnz .LBB0_1252
	s_and_b32 s99, s94, 7
	s_lshl_b32 s99, s99, 5
	s_lshr_b32 s94, s94, 3
	s_or_b32 s94, s94, s99
	s_mov_b32 s99, 0
	v_readlane_b32 s0, v252, 0
	s_lshl_b32 s0, s0, 6
	s_sub_i32 s0, 0, s0
	s_waitcnt vmcnt(0)
	v_mbcnt_lo_u32_b32 v0, -1, 0
	v_mbcnt_hi_u32_b32 v0, -1, v0
	s_nop 0
	v_cmp_eq_u32_e32 vcc, s0, v0
	s_and_saveexec_b64 s[0:1], vcc
	s_cbranch_execz .LBB0_1131
	v_mov_b32_e32 v9, 0x4000
	s_waitcnt lgkmcnt(0)
	global_load_dwordx4 v[0:3], v9, s[76:77]
	global_load_dwordx4 v[4:7], v9, s[76:77] offset:60
	s_add_u32 s2, s76, 0x4000
	v_mov_b32_e32 v8, 0
	s_addc_u32 s3, s77, 0
	global_load_dwordx4 v[10:13], v8, s[2:3] offset:16
	global_load_dwordx4 v[14:17], v8, s[2:3] offset:32
	global_load_dwordx3 v[36:38], v8, s[2:3] offset:48
	s_add_i32 s2, 0, 0x20400
	s_add_i32 s3, 0, 0x20490
	s_add_i32 s6, 0, 0x20410
	s_add_i32 s7, 0, 0x204a0
	s_add_i32 s8, 0, 0x20420
	s_add_i32 s9, 0, 0x204b0
	v_mov_b32_e32 v39, s2
	s_add_u32 s2, s76, 0x403c
	v_mov_b32_e32 v40, s3
	s_addc_u32 s3, s77, 0
	global_load_dword v45, v9, s[76:77] offset:124
	global_load_dwordx4 v[18:21], v8, s[2:3] offset:48
	global_load_dwordx4 v[22:25], v8, s[2:3] offset:32
	global_load_dwordx4 v[26:29], v8, s[2:3] offset:16
	v_mov_b32_e32 v41, s6
	v_mov_b32_e32 v42, s7
	v_mov_b32_e32 v43, s8
	s_add_i32 s6, 0, 0x20430
	v_mov_b32_e32 v46, s6
	s_add_i32 s2, 0, 0x204c0
	v_mov_b32_e32 v44, s9
	s_waitcnt vmcnt(8)
	v_add_u32_e32 v9, 0xff, v0
	v_add_u32_e32 v31, 0xff, v1
	v_add_u32_e32 v32, 0xff, v2
	v_add_u32_e32 v33, 0xff, v3
	v_ashrrev_i32_e32 v9, 8, v9
	v_ashrrev_i32_e32 v49, 8, v31
	v_mov_b32_e32 v30, v3
	v_ashrrev_i32_e32 v50, 8, v32
	v_ashrrev_i32_e32 v51, 8, v33
	s_waitcnt vmcnt(6)
	v_add_u32_e32 v52, 0xff, v10
	v_add_u32_e32 v53, 0xff, v11
	v_mov_b32_e32 v31, v10
	v_mov_b32_e32 v32, v11
	v_mov_b32_e32 v33, v12
	v_add_u32_e32 v11, 0xff, v12
	v_add_u32_e32 v10, v49, v9
	v_add_u32_e32 v47, 0xff, v5
	ds_write_b128 v40, v[30:33]
	v_ashrrev_i32_e32 v30, 8, v11
	v_add_u32_e32 v11, v50, v10
	s_waitcnt vmcnt(5)
	v_add_u32_e32 v57, 0xff, v17
	s_waitcnt vmcnt(4)
	v_add_u32_e32 v58, 0xff, v36
	v_add_u32_e32 v59, 0xff, v37
	v_mov_b32_e32 v34, v17
	v_mov_b32_e32 v35, v36
	v_mov_b32_e32 v36, v37
	v_mov_b32_e32 v37, v38
	v_add_u32_e32 v17, 0xff, v38
	v_ashrrev_i32_e32 v38, 8, v47
	v_ashrrev_i32_e32 v47, 8, v52
	ds_write_b128 v39, v[8:11]
	v_add_u32_e32 v8, v51, v11
	v_ashrrev_i32_e32 v49, 8, v53
	v_add_u32_e32 v9, v47, v8
	v_add_u32_e32 v54, 0xff, v13
	v_add_u32_e32 v10, v49, v9
	v_add_u32_e32 v55, 0xff, v14
	v_ashrrev_i32_e32 v31, 8, v54
	v_add_u32_e32 v11, v30, v10
	v_add_u32_e32 v56, 0xff, v15
	v_ashrrev_i32_e32 v32, 8, v55
	ds_write_b128 v41, v[8:11]
	v_add_u32_e32 v8, v31, v11
	v_mov_b32_e32 v12, v13
	v_mov_b32_e32 v13, v14
	v_mov_b32_e32 v14, v15
	v_mov_b32_e32 v15, v16
	v_add_u32_e32 v16, 0xff, v16
	v_ashrrev_i32_e32 v33, 8, v56
	v_add_u32_e32 v9, v32, v8
	ds_write_b128 v42, v[12:15]
	v_ashrrev_i32_e32 v12, 8, v16
	v_add_u32_e32 v10, v33, v9
	v_ashrrev_i32_e32 v13, 8, v57
	v_add_u32_e32 v11, v12, v10
	v_ashrrev_i32_e32 v14, 8, v58
	ds_write_b128 v43, v[8:11]
	v_add_u32_e32 v8, v13, v11
	v_ashrrev_i32_e32 v15, 8, v59
	v_add_u32_e32 v9, v14, v8
	v_add_u32_e32 v3, 0xff, v4
	v_ashrrev_i32_e32 v16, 8, v17
	v_add_u32_e32 v10, v15, v9
	v_ashrrev_i32_e32 v3, 8, v3
	v_add_u32_e32 v11, v16, v10
	v_add_u32_e32 v48, 0xff, v6
	ds_write_b128 v46, v[8:11]
	v_add_u32_e32 v8, v3, v11
	v_add_u32_e32 v9, v38, v8
	v_ashrrev_i32_e32 v3, 8, v48
	v_add_u32_e32 v10, v3, v9
	v_mov_b32_e32 v3, s2
	ds_write_b128 v3, v[4:7]
	v_add_u32_e32 v3, 0xff, v7
	v_ashrrev_i32_e32 v3, 8, v3
	s_add_i32 s2, 0, 0x20440
	v_add_u32_e32 v11, v3, v10
	v_mov_b32_e32 v3, s2
	ds_write_b128 v3, v[8:11]
	s_waitcnt vmcnt(0)
	v_add_u32_e32 v3, 0xff, v26
	v_ashrrev_i32_e32 v3, 8, v3
	v_add_u32_e32 v4, v3, v11
	v_add_u32_e32 v3, 0xff, v27
	v_ashrrev_i32_e32 v3, 8, v3
	v_add_u32_e32 v5, v3, v4
	v_add_u32_e32 v3, 0xff, v28
	v_ashrrev_i32_e32 v3, 8, v3
	s_add_i32 s2, 0, 0x204d0
	v_add_u32_e32 v6, v3, v5
	v_mov_b32_e32 v3, s2
	ds_write_b128 v3, v[26:29]
	v_add_u32_e32 v3, 0xff, v29
	v_ashrrev_i32_e32 v3, 8, v3
	s_add_i32 s2, 0, 0x20450
	v_add_u32_e32 v7, v3, v6
	v_mov_b32_e32 v3, s2
	ds_write_b128 v3, v[4:7]
	v_add_u32_e32 v3, 0xff, v22
	v_ashrrev_i32_e32 v3, 8, v3
	v_add_u32_e32 v4, v3, v7
	v_add_u32_e32 v3, 0xff, v23
	v_ashrrev_i32_e32 v3, 8, v3
	v_add_u32_e32 v5, v3, v4
	v_add_u32_e32 v3, 0xff, v24
	v_ashrrev_i32_e32 v3, 8, v3
	s_add_i32 s2, 0, 0x204e0
	v_add_u32_e32 v6, v3, v5
	v_mov_b32_e32 v3, s2
	ds_write_b128 v3, v[22:25]
	v_add_u32_e32 v3, 0xff, v25
	v_ashrrev_i32_e32 v3, 8, v3
	s_add_i32 s2, 0, 0x20460
	v_add_u32_e32 v7, v3, v6
	v_mov_b32_e32 v3, s2
	ds_write_b128 v3, v[4:7]
	v_add_u32_e32 v3, 0xff, v18
	v_ashrrev_i32_e32 v3, 8, v3
	v_add_u32_e32 v4, v3, v7
	v_add_u32_e32 v3, 0xff, v19
	v_ashrrev_i32_e32 v3, 8, v3
	v_add_u32_e32 v5, v3, v4
	v_add_u32_e32 v3, 0xff, v20
	v_ashrrev_i32_e32 v3, 8, v3
	s_add_i32 s2, 0, 0x204f0
	v_add_u32_e32 v6, v3, v5
	v_mov_b32_e32 v3, s2
	ds_write_b128 v3, v[18:21]
	v_add_u32_e32 v3, 0xff, v21
	v_ashrrev_i32_e32 v3, 8, v3
	s_add_i32 s2, 0, 0x20470
	v_add_u32_e32 v7, v3, v6
	v_mov_b32_e32 v3, s2
	s_add_i32 s2, 0, 0x20500
	ds_write_b128 v3, v[4:7]
	v_mov_b32_e32 v3, s2
	ds_write_b32 v3, v45
	v_add_u32_e32 v3, 0xff, v45
	v_ashrrev_i32_e32 v3, 8, v3
	s_add_i32 s2, 0, 0x20480
	v_add_u32_e32 v4, v3, v7
	v_mov_b32_e32 v5, v0
	v_mov_b32_e32 v6, v1
	v_mov_b32_e32 v7, v2
	v_mov_b32_e32 v0, s2
	ds_write_b128 v44, v[34:37]
	ds_write_b128 v0, v[4:7]

; #define LAS __attribute__((address_space(3)))
; __device__ __forceinline__ int mk_tid(const int wv) { int ln; asm volatile("v_mbcnt_lo_u32_b32 %0, -1, 0\n\tv_mbcnt_hi_u32_b32 %0, -1, %0" : "=v"(ln)); return wv * 64 + ln; }
; __device__ __forceinline__ void moe_tiles(const int* cnt, LAS int* tb, const int wv) {
;     if (mk_tid(wv) == 0) { int acc = 0; for (int e = 0; e < 32; ++e) { const int c = cnt[e]; tb[e] = acc; tb[33 + e] = c; acc += (c + 255) >> 8; } tb[32] = acc; }
;     __syncthreads();
; }
.LBB0_2038:
	s_cmp_lt_i32 s78, 14
	s_cselect_b64 s[4:5], -1, 0
	s_and_b64 s[0:1], s[4:5], s[0:1]
	s_andn2_b64 vcc, exec, s[0:1]
	s_cbranch_vccnz .LBB0_2129
	s_and_b32 s99, s94, 7
	s_lshl_b32 s99, s99, 5
	s_lshr_b32 s94, s94, 3
	s_or_b32 s94, s94, s99
	s_mov_b32 s99, 0
	v_readlane_b32 s0, v252, 0
	s_lshl_b32 s0, s0, 6
	s_sub_i32 s0, 0, s0
	s_waitcnt vmcnt(0)
	v_mbcnt_lo_u32_b32 v0, -1, 0
	v_mbcnt_hi_u32_b32 v0, -1, v0
	s_nop 0
	v_cmp_eq_u32_e32 vcc, s0, v0
	s_and_saveexec_b64 s[0:1], vcc
	s_cbranch_execz .LBB0_2041
	v_mov_b32_e32 v9, 0x4000
	s_waitcnt lgkmcnt(0)
	global_load_dwordx4 v[0:3], v9, s[76:77] offset:128
	global_load_dwordx4 v[4:7], v9, s[76:77] offset:188
	s_add_u32 s2, s76, 0x4080
	v_mov_b32_e32 v8, 0
	s_addc_u32 s3, s77, 0
	global_load_dwordx4 v[10:13], v8, s[2:3] offset:16
	global_load_dwordx4 v[14:17], v8, s[2:3] offset:32
	global_load_dwordx3 v[36:38], v8, s[2:3] offset:48
	s_add_i32 s2, 0, 0x20400
	s_add_i32 s3, 0, 0x20490
	s_add_i32 s6, 0, 0x20410
	s_add_i32 s7, 0, 0x204a0
	s_add_i32 s8, 0, 0x20420
	s_add_i32 s9, 0, 0x204b0
	v_mov_b32_e32 v39, s2
	s_add_u32 s2, s76, 0x40bc
	v_mov_b32_e32 v40, s3
	s_addc_u32 s3, s77, 0
	global_load_dword v45, v9, s[76:77] offset:252
	global_load_dwordx4 v[18:21], v8, s[2:3] offset:48
	global_load_dwordx4 v[22:25], v8, s[2:3] offset:32
	global_load_dwordx4 v[26:29], v8, s[2:3] offset:16
	v_mov_b32_e32 v41, s6
	v_mov_b32_e32 v42, s7
	v_mov_b32_e32 v43, s8
	s_add_i32 s6, 0, 0x20430
	v_mov_b32_e32 v46, s6
	s_add_i32 s2, 0, 0x204c0
	v_mov_b32_e32 v44, s9
	s_waitcnt vmcnt(8)
	v_add_u32_e32 v9, 0xff, v0
	v_add_u32_e32 v31, 0xff, v1
	v_add_u32_e32 v32, 0xff, v2
	v_add_u32_e32 v33, 0xff, v3
	v_ashrrev_i32_e32 v9, 8, v9
	v_ashrrev_i32_e32 v49, 8, v31
	v_mov_b32_e32 v30, v3
	v_ashrrev_i32_e32 v50, 8, v32
	v_ashrrev_i32_e32 v51, 8, v33
	s_waitcnt vmcnt(6)
	v_add_u32_e32 v52, 0xff, v10
	v_add_u32_e32 v53, 0xff, v11
	v_mov_b32_e32 v31, v10
	v_mov_b32_e32 v32, v11
	v_mov_b32_e32 v33, v12
	v_add_u32_e32 v11, 0xff, v12
	v_add_u32_e32 v10, v49, v9
	v_add_u32_e32 v47, 0xff, v5
	ds_write_b128 v40, v[30:33]
	v_ashrrev_i32_e32 v30, 8, v11
	v_add_u32_e32 v11, v50, v10
	s_waitcnt vmcnt(5)
	v_add_u32_e32 v57, 0xff, v17
	s_waitcnt vmcnt(4)
	v_add_u32_e32 v58, 0xff, v36
	v_add_u32_e32 v59, 0xff, v37
	v_mov_b32_e32 v34, v17
	v_mov_b32_e32 v35, v36
	v_mov_b32_e32 v36, v37
	v_mov_b32_e32 v37, v38
	v_add_u32_e32 v17, 0xff, v38
	v_ashrrev_i32_e32 v38, 8, v47
	v_ashrrev_i32_e32 v47, 8, v52
	ds_write_b128 v39, v[8:11]
	v_add_u32_e32 v8, v51, v11
	v_ashrrev_i32_e32 v49, 8, v53
	v_add_u32_e32 v9, v47, v8
	v_add_u32_e32 v54, 0xff, v13
	v_add_u32_e32 v10, v49, v9
	v_add_u32_e32 v55, 0xff, v14
	v_ashrrev_i32_e32 v31, 8, v54
	v_add_u32_e32 v11, v30, v10
	v_add_u32_e32 v56, 0xff, v15
	v_ashrrev_i32_e32 v32, 8, v55
	ds_write_b128 v41, v[8:11]
	v_add_u32_e32 v8, v31, v11
	v_mov_b32_e32 v12, v13
	v_mov_b32_e32 v13, v14
	v_mov_b32_e32 v14, v15
	v_mov_b32_e32 v15, v16
	v_add_u32_e32 v16, 0xff, v16
	v_ashrrev_i32_e32 v33, 8, v56
	v_add_u32_e32 v9, v32, v8
	ds_write_b128 v42, v[12:15]
	v_ashrrev_i32_e32 v12, 8, v16
	v_add_u32_e32 v10, v33, v9
	v_ashrrev_i32_e32 v13, 8, v57
	v_add_u32_e32 v11, v12, v10
	v_ashrrev_i32_e32 v14, 8, v58
	ds_write_b128 v43, v[8:11]
	v_add_u32_e32 v8, v13, v11
	v_ashrrev_i32_e32 v15, 8, v59
	v_add_u32_e32 v9, v14, v8
	v_add_u32_e32 v3, 0xff, v4
	v_ashrrev_i32_e32 v16, 8, v17
	v_add_u32_e32 v10, v15, v9
	v_ashrrev_i32_e32 v3, 8, v3
	v_add_u32_e32 v11, v16, v10
	v_add_u32_e32 v48, 0xff, v6
	ds_write_b128 v46, v[8:11]
	v_add_u32_e32 v8, v3, v11
	v_add_u32_e32 v9, v38, v8
	v_ashrrev_i32_e32 v3, 8, v48
	v_add_u32_e32 v10, v3, v9
	v_mov_b32_e32 v3, s2
	ds_write_b128 v3, v[4:7]
	v_add_u32_e32 v3, 0xff, v7
	v_ashrrev_i32_e32 v3, 8, v3
	s_add_i32 s2, 0, 0x20440
	v_add_u32_e32 v11, v3, v10
	v_mov_b32_e32 v3, s2
	ds_write_b128 v3, v[8:11]
	s_waitcnt vmcnt(0)
	v_add_u32_e32 v3, 0xff, v26
	v_ashrrev_i32_e32 v3, 8, v3
	v_add_u32_e32 v4, v3, v11
	v_add_u32_e32 v3, 0xff, v27
	v_ashrrev_i32_e32 v3, 8, v3
	v_add_u32_e32 v5, v3, v4
	v_add_u32_e32 v3, 0xff, v28
	v_ashrrev_i32_e32 v3, 8, v3
	s_add_i32 s2, 0, 0x204d0
	v_add_u32_e32 v6, v3, v5
	v_mov_b32_e32 v3, s2
	ds_write_b128 v3, v[26:29]
	v_add_u32_e32 v3, 0xff, v29
	v_ashrrev_i32_e32 v3, 8, v3
	s_add_i32 s2, 0, 0x20450
	v_add_u32_e32 v7, v3, v6
	v_mov_b32_e32 v3, s2
	ds_write_b128 v3, v[4:7]
	v_add_u32_e32 v3, 0xff, v22
	v_ashrrev_i32_e32 v3, 8, v3
	v_add_u32_e32 v4, v3, v7
	v_add_u32_e32 v3, 0xff, v23
	v_ashrrev_i32_e32 v3, 8, v3
	v_add_u32_e32 v5, v3, v4
	v_add_u32_e32 v3, 0xff, v24
	v_ashrrev_i32_e32 v3, 8, v3
	s_add_i32 s2, 0, 0x204e0
	v_add_u32_e32 v6, v3, v5
	v_mov_b32_e32 v3, s2
	ds_write_b128 v3, v[22:25]
	v_add_u32_e32 v3, 0xff, v25
	v_ashrrev_i32_e32 v3, 8, v3
	s_add_i32 s2, 0, 0x20460
	v_add_u32_e32 v7, v3, v6
	v_mov_b32_e32 v3, s2
	ds_write_b128 v3, v[4:7]
	v_add_u32_e32 v3, 0xff, v18
	v_ashrrev_i32_e32 v3, 8, v3
	v_add_u32_e32 v4, v3, v7
	v_add_u32_e32 v3, 0xff, v19
	v_ashrrev_i32_e32 v3, 8, v3
	v_add_u32_e32 v5, v3, v4
	v_add_u32_e32 v3, 0xff, v20
	v_ashrrev_i32_e32 v3, 8, v3
	s_add_i32 s2, 0, 0x204f0
	v_add_u32_e32 v6, v3, v5
	v_mov_b32_e32 v3, s2
	ds_write_b128 v3, v[18:21]
	v_add_u32_e32 v3, 0xff, v21
	v_ashrrev_i32_e32 v3, 8, v3
	s_add_i32 s2, 0, 0x20470
	v_add_u32_e32 v7, v3, v6
	v_mov_b32_e32 v3, s2
	s_add_i32 s2, 0, 0x20500
	ds_write_b128 v3, v[4:7]
	v_mov_b32_e32 v3, s2
	ds_write_b32 v3, v45
	v_add_u32_e32 v3, 0xff, v45
	v_ashrrev_i32_e32 v3, 8, v3
	s_add_i32 s2, 0, 0x20480
	v_add_u32_e32 v4, v3, v7
	v_mov_b32_e32 v5, v0
	v_mov_b32_e32 v6, v1
	v_mov_b32_e32 v7, v2
	v_mov_b32_e32 v0, s2
	ds_write_b128 v44, v[34:37]
	ds_write_b128 v0, v[4:7]

; #define LAS __attribute__((address_space(3)))
; __device__ __forceinline__ int mk_tid(const int wv) { int ln; asm volatile("v_mbcnt_lo_u32_b32 %0, -1, 0\n\tv_mbcnt_hi_u32_b32 %0, -1, %0" : "=v"(ln)); return wv * 64 + ln; }
; __device__ __forceinline__ void moe_tiles(const int* cnt, LAS int* tb, const int wv) {
;     if (mk_tid(wv) == 0) { int acc = 0; for (int e = 0; e < 32; ++e) { const int c = cnt[e]; tb[e] = acc; tb[33 + e] = c; acc += (c + 255) >> 8; } tb[32] = acc; }
;     __syncthreads();
; }
.LBB0_2179:
	s_cmp_lt_i32 s78, 15
	s_cselect_b64 s[4:5], -1, 0
	s_and_b64 s[0:1], s[4:5], s[0:1]
	s_andn2_b64 vcc, exec, s[0:1]
	s_cbranch_vccnz .LBB0_2241
	s_and_b32 s99, s94, 7
	s_lshl_b32 s99, s99, 5
	s_lshr_b32 s94, s94, 3
	s_or_b32 s94, s94, s99
	s_mov_b32 s99, 0
	v_readlane_b32 s0, v252, 0
	s_lshl_b32 s0, s0, 6
	s_sub_i32 s0, 0, s0
	s_waitcnt vmcnt(0)
	v_mbcnt_lo_u32_b32 v0, -1, 0
	v_mbcnt_hi_u32_b32 v0, -1, v0
	s_nop 0
	v_cmp_eq_u32_e32 vcc, s0, v0
	s_and_saveexec_b64 s[0:1], vcc
	s_cbranch_execz .LBB0_2182
	v_mov_b32_e32 v9, 0x4000
	s_waitcnt lgkmcnt(0)
	global_load_dwordx4 v[0:3], v9, s[76:77] offset:128
	global_load_dwordx4 v[4:7], v9, s[76:77] offset:188
	s_add_u32 s2, s76, 0x4080
	v_mov_b32_e32 v8, 0
	s_addc_u32 s3, s77, 0
	global_load_dwordx4 v[10:13], v8, s[2:3] offset:16
	global_load_dwordx4 v[14:17], v8, s[2:3] offset:32
	global_load_dwordx3 v[36:38], v8, s[2:3] offset:48
	s_add_i32 s2, 0, 0x20400
	s_add_i32 s3, 0, 0x20490
	s_add_i32 s6, 0, 0x20410
	s_add_i32 s7, 0, 0x204a0
	s_add_i32 s8, 0, 0x20420
	s_add_i32 s9, 0, 0x204b0
	v_mov_b32_e32 v39, s2
	s_add_u32 s2, s76, 0x40bc
	v_mov_b32_e32 v40, s3
	s_addc_u32 s3, s77, 0
	global_load_dword v45, v9, s[76:77] offset:252
	global_load_dwordx4 v[18:21], v8, s[2:3] offset:48
	global_load_dwordx4 v[22:25], v8, s[2:3] offset:32
	global_load_dwordx4 v[26:29], v8, s[2:3] offset:16
	v_mov_b32_e32 v41, s6
	v_mov_b32_e32 v42, s7
	v_mov_b32_e32 v43, s8
	s_add_i32 s6, 0, 0x20430
	v_mov_b32_e32 v46, s6
	s_add_i32 s2, 0, 0x204c0
	v_mov_b32_e32 v44, s9
	s_waitcnt vmcnt(8)
	v_add_u32_e32 v9, 0xff, v0
	v_add_u32_e32 v31, 0xff, v1
	v_add_u32_e32 v32, 0xff, v2
	v_add_u32_e32 v33, 0xff, v3
	v_ashrrev_i32_e32 v9, 8, v9
	v_ashrrev_i32_e32 v49, 8, v31
	v_mov_b32_e32 v30, v3
	v_ashrrev_i32_e32 v50, 8, v32
	v_ashrrev_i32_e32 v51, 8, v33
	s_waitcnt vmcnt(6)
	v_add_u32_e32 v52, 0xff, v10
	v_add_u32_e32 v53, 0xff, v11
	v_mov_b32_e32 v31, v10
	v_mov_b32_e32 v32, v11
	v_mov_b32_e32 v33, v12
	v_add_u32_e32 v11, 0xff, v12
	v_add_u32_e32 v10, v49, v9
	v_add_u32_e32 v47, 0xff, v5
	ds_write_b128 v40, v[30:33]
	v_ashrrev_i32_e32 v30, 8, v11
	v_add_u32_e32 v11, v50, v10
	s_waitcnt vmcnt(5)
	v_add_u32_e32 v57, 0xff, v17
	s_waitcnt vmcnt(4)
	v_add_u32_e32 v58, 0xff, v36
	v_add_u32_e32 v59, 0xff, v37
	v_mov_b32_e32 v34, v17
	v_mov_b32_e32 v35, v36
	v_mov_b32_e32 v36, v37
	v_mov_b32_e32 v37, v38
	v_add_u32_e32 v17, 0xff, v38
	v_ashrrev_i32_e32 v38, 8, v47
	v_ashrrev_i32_e32 v47, 8, v52
	ds_write_b128 v39, v[8:11]
	v_add_u32_e32 v8, v51, v11
	v_ashrrev_i32_e32 v49, 8, v53
	v_add_u32_e32 v9, v47, v8
	v_add_u32_e32 v54, 0xff, v13
	v_add_u32_e32 v10, v49, v9
	v_add_u32_e32 v55, 0xff, v14
	v_ashrrev_i32_e32 v31, 8, v54
	v_add_u32_e32 v11, v30, v10
	v_add_u32_e32 v56, 0xff, v15
	v_ashrrev_i32_e32 v32, 8, v55
	ds_write_b128 v41, v[8:11]
	v_add_u32_e32 v8, v31, v11
	v_mov_b32_e32 v12, v13
	v_mov_b32_e32 v13, v14
	v_mov_b32_e32 v14, v15
	v_mov_b32_e32 v15, v16
	v_add_u32_e32 v16, 0xff, v16
	v_ashrrev_i32_e32 v33, 8, v56
	v_add_u32_e32 v9, v32, v8
	ds_write_b128 v42, v[12:15]
	v_ashrrev_i32_e32 v12, 8, v16
	v_add_u32_e32 v10, v33, v9
	v_ashrrev_i32_e32 v13, 8, v57
	v_add_u32_e32 v11, v12, v10
	v_ashrrev_i32_e32 v14, 8, v58
	ds_write_b128 v43, v[8:11]
	v_add_u32_e32 v8, v13, v11
	v_ashrrev_i32_e32 v15, 8, v59
	v_add_u32_e32 v9, v14, v8
	v_add_u32_e32 v3, 0xff, v4
	v_ashrrev_i32_e32 v16, 8, v17
	v_add_u32_e32 v10, v15, v9
	v_ashrrev_i32_e32 v3, 8, v3
	v_add_u32_e32 v11, v16, v10
	v_add_u32_e32 v48, 0xff, v6
	ds_write_b128 v46, v[8:11]
	v_add_u32_e32 v8, v3, v11
	v_add_u32_e32 v9, v38, v8
	v_ashrrev_i32_e32 v3, 8, v48
	v_add_u32_e32 v10, v3, v9
	v_mov_b32_e32 v3, s2
	ds_write_b128 v3, v[4:7]
	v_add_u32_e32 v3, 0xff, v7
	v_ashrrev_i32_e32 v3, 8, v3
	s_add_i32 s2, 0, 0x20440
	v_add_u32_e32 v11, v3, v10
	v_mov_b32_e32 v3, s2
	ds_write_b128 v3, v[8:11]
	s_waitcnt vmcnt(0)
	v_add_u32_e32 v3, 0xff, v26
	v_ashrrev_i32_e32 v3, 8, v3
	v_add_u32_e32 v4, v3, v11
	v_add_u32_e32 v3, 0xff, v27
	v_ashrrev_i32_e32 v3, 8, v3
	v_add_u32_e32 v5, v3, v4
	v_add_u32_e32 v3, 0xff, v28
	v_ashrrev_i32_e32 v3, 8, v3
	s_add_i32 s2, 0, 0x204d0
	v_add_u32_e32 v6, v3, v5
	v_mov_b32_e32 v3, s2
	ds_write_b128 v3, v[26:29]
	v_add_u32_e32 v3, 0xff, v29
	v_ashrrev_i32_e32 v3, 8, v3
	s_add_i32 s2, 0, 0x20450
	v_add_u32_e32 v7, v3, v6
	v_mov_b32_e32 v3, s2
	ds_write_b128 v3, v[4:7]
	v_add_u32_e32 v3, 0xff, v22
	v_ashrrev_i32_e32 v3, 8, v3
	v_add_u32_e32 v4, v3, v7
	v_add_u32_e32 v3, 0xff, v23
	v_ashrrev_i32_e32 v3, 8, v3
	v_add_u32_e32 v5, v3, v4
	v_add_u32_e32 v3, 0xff, v24
	v_ashrrev_i32_e32 v3, 8, v3
	s_add_i32 s2, 0, 0x204e0
	v_add_u32_e32 v6, v3, v5
	v_mov_b32_e32 v3, s2
	ds_write_b128 v3, v[22:25]
	v_add_u32_e32 v3, 0xff, v25
	v_ashrrev_i32_e32 v3, 8, v3
	s_add_i32 s2, 0, 0x20460
	v_add_u32_e32 v7, v3, v6
	v_mov_b32_e32 v3, s2
	ds_write_b128 v3, v[4:7]
	v_add_u32_e32 v3, 0xff, v18
	v_ashrrev_i32_e32 v3, 8, v3
	v_add_u32_e32 v4, v3, v7
	v_add_u32_e32 v3, 0xff, v19
	v_ashrrev_i32_e32 v3, 8, v3
	v_add_u32_e32 v5, v3, v4
	v_add_u32_e32 v3, 0xff, v20
	v_ashrrev_i32_e32 v3, 8, v3
	s_add_i32 s2, 0, 0x204f0
	v_add_u32_e32 v6, v3, v5
	v_mov_b32_e32 v3, s2
	ds_write_b128 v3, v[18:21]
	v_add_u32_e32 v3, 0xff, v21
	v_ashrrev_i32_e32 v3, 8, v3
	s_add_i32 s2, 0, 0x20470
	v_add_u32_e32 v7, v3, v6
	v_mov_b32_e32 v3, s2
	s_add_i32 s2, 0, 0x20500
	ds_write_b128 v3, v[4:7]
	v_mov_b32_e32 v3, s2
	ds_write_b32 v3, v45
	v_add_u32_e32 v3, 0xff, v45
	v_ashrrev_i32_e32 v3, 8, v3
	s_add_i32 s2, 0, 0x20480
	v_add_u32_e32 v4, v3, v7
	v_mov_b32_e32 v5, v0
	v_mov_b32_e32 v6, v1
	v_mov_b32_e32 v7, v2
	v_mov_b32_e32 v0, s2
	ds_write_b128 v44, v[34:37]
	ds_write_b128 v0, v[4:7]
